# speedup vs baseline: 1.0042x; 1.0042x over previous
_Z6conv_kILi512ELi256ELi3ELi64ELi1ELi1ELb0EEvPKDF16_S1_PKfS3_PDF16_S4_S1_fS3_S3_S3_S3_:
	s_lshl_b32 s3, s2, 3
	s_load_dwordx2 s[36:37], s[0:1], 0x0
	s_load_dwordx4 s[4:7], s[0:1], 0x10
	s_load_dwordx2 s[30:31], s[0:1], 0x30
	s_and_b32 s3, s3, 56
	s_ashr_i32 s8, s2, 5
	s_add_i32 s3, s3, s8
	v_readfirstlane_b32 s42, v0
	s_lshl_b32 s8, s3, 2
	s_bfe_u32 s38, s2, 0x20003
	s_and_b32 s33, s8, 56
	s_lshr_b32 s52, s42, 6
	s_ashr_i32 s40, s3, 4
	s_and_b32 s27, s2, 32
	s_lshl_b32 s2, s38, 8
	v_bfe_u32 v29, v0, 3, 3
	v_and_b32_e32 v2, 7, v0
	s_waitcnt lgkmcnt(0)
	s_add_u32 s2, s4, s2
	v_bitop3_b32 v2, v29, v2, 6 bitop3:0x6c
	s_addc_u32 s3, s5, 0
	v_and_b32_e32 v18, 48, v0
	v_mov_b32_e32 v19, 0
	v_lshlrev_b32_e32 v20, 3, v2
	v_lshl_add_u64 v[2:3], s[2:3], 0, v[18:19]
	s_load_dword s26, s[6:7], 0x0
	global_load_dwordx4 v[14:17], v[2:3], off
	v_lshl_add_u64 v[4:5], v[2:3], 0, 64
	s_mov_b64 s[2:3], 0x80
	global_load_dwordx4 v[10:13], v[4:5], off
	v_lshl_add_u64 v[4:5], v[2:3], 0, s[2:3]
	s_mov_b64 s[2:3], 0xc0
	v_lshl_add_u64 v[2:3], v[2:3], 0, s[2:3]
	v_lshl_or_b32 v18, s52, 3, v29
	s_mov_b32 s2, 0x1e1e1e1f
	v_mul_hi_u32 v21, v18, s2
	v_lshrrev_b32_e32 v21, 2, v21
	s_movk_i32 s8, 0xffde
	s_add_i32 s24, s33, -1
	global_load_dwordx4 v[6:9], v[4:5], off
	v_mul_lo_u32 v22, v21, s8
	v_add_u32_e32 v25, s24, v21
	s_add_i32 s25, s27, -1
	s_movk_i32 s9, 0x154
	global_load_dwordx4 v[2:5], v[2:3], off
	v_add3_u32 v24, s25, v18, v22
	v_cmp_gt_u32_e64 s[2:3], s9, v18
	v_cmp_gt_u32_e32 vcc, 64, v25
	s_and_b64 s[6:7], s[2:3], vcc
	v_cmp_gt_u32_e64 s[4:5], 64, v24
	v_and_b32_e32 v1, 63, v0
	s_and_b64 s[10:11], s[6:7], s[4:5]
	v_mov_b64_e32 v[22:23], s[30:31]
	v_lshlrev_b32_e32 v18, 1, v20
	s_and_saveexec_b64 s[6:7], s[10:11]
	s_lshl_b32 s10, s40, 15
	v_lshlrev_b32_e32 v22, 6, v25
	v_or3_b32 v22, v22, s10, v24
	v_ashrrev_i32_e32 v23, 31, v22
	v_lshlrev_b64 v[22:23], 7, v[22:23]
	v_lshl_add_u64 v[22:23], s[36:37], 0, v[22:23]
	v_lshl_add_u64 v[22:23], v[22:23], 0, v[18:19]
	s_or_b64 exec, exec, s[6:7]
	s_lshl_b32 s43, s52, 10
	v_lshlrev_b32_e32 v120, 4, v1
	v_or_b32_e32 v19, s43, v120
	s_add_i32 s13, s52, 8
	v_readfirstlane_b32 s6, v19
	s_mov_b32 m0, s6
	s_mov_b32 s12, 0x3c3c3c3d
	v_mov_b64_e32 v[184:185], v[22:23]
	global_load_lds_dwordx4 v[22:23], off
	v_lshl_or_b32 v22, s13, 3, v29
	v_mul_hi_u32 v19, v22, s12
	v_lshrrev_b32_e32 v25, 3, v19
	v_mul_lo_u32 v23, v25, s8
	v_add_u32_e32 v19, s24, v25
	v_add3_u32 v26, s25, v22, v23
	v_cmp_gt_u32_e64 s[6:7], s9, v22
	v_cmp_gt_u32_e32 vcc, 64, v19
	s_and_b64 s[10:11], s[6:7], vcc
	v_cmp_gt_u32_e64 s[8:9], 64, v26
	s_and_b64 s[14:15], s[10:11], s[8:9]
	v_mov_b64_e32 v[22:23], s[30:31]
	s_and_saveexec_b64 s[10:11], s[14:15]
	s_lshl_b32 s14, s40, 15
	v_lshlrev_b32_e32 v19, 6, v19
	v_or3_b32 v22, v19, s14, v26
	v_ashrrev_i32_e32 v23, 31, v22
	v_lshlrev_b64 v[22:23], 7, v[22:23]
	v_lshl_add_u64 v[22:23], s[36:37], 0, v[22:23]
	v_mov_b32_e32 v19, 0
	v_lshl_add_u64 v[22:23], v[22:23], 0, v[18:19]
	s_or_b64 exec, exec, s[10:11]
	s_lshl_b32 s44, s13, 10
	v_or_b32_e32 v19, s44, v120
	s_add_i32 s18, s52, 16
	v_readfirstlane_b32 s10, v19
	s_mov_b32 m0, s10
	s_movk_i32 s16, 0xffde
	v_mov_b64_e32 v[186:187], v[22:23]
	global_load_lds_dwordx4 v[22:23], off
	v_lshl_or_b32 v22, s18, 3, v29
	v_mul_hi_u32 v19, v22, s12
	v_lshrrev_b32_e32 v27, 3, v19
	v_mul_lo_u32 v23, v27, s16
	v_add_u32_e32 v19, s24, v27
	s_movk_i32 s17, 0x154
	v_add3_u32 v28, s25, v22, v23
	v_cmp_gt_u32_e64 s[10:11], s17, v22
	v_cmp_gt_u32_e32 vcc, 64, v19
	s_and_b64 s[14:15], s[10:11], vcc
	v_cmp_gt_u32_e64 s[12:13], 64, v28
	s_and_b64 s[20:21], s[14:15], s[12:13]
	v_mov_b64_e32 v[22:23], s[30:31]
	s_and_saveexec_b64 s[14:15], s[20:21]
	s_lshl_b32 s19, s40, 15
	v_lshlrev_b32_e32 v19, 6, v19
	v_or3_b32 v22, v19, s19, v28
	v_ashrrev_i32_e32 v23, 31, v22
	v_lshlrev_b64 v[22:23], 7, v[22:23]
	v_lshl_add_u64 v[22:23], s[36:37], 0, v[22:23]
	v_mov_b32_e32 v19, 0
	v_lshl_add_u64 v[22:23], v[22:23], 0, v[18:19]
	s_or_b64 exec, exec, s[14:15]
	s_lshl_b32 s45, s18, 10
	v_or_b32_e32 v19, s45, v120
	s_add_i32 s21, s52, 24
	v_readfirstlane_b32 s14, v19
	s_mov_b32 m0, s14
	s_mov_b32 s20, 0x3c3c3c3d
	v_mov_b64_e32 v[188:189], v[22:23]
	global_load_lds_dwordx4 v[22:23], off
	v_lshl_or_b32 v22, s21, 3, v29
	v_mul_hi_u32 v19, v22, s20
	v_lshrrev_b32_e32 v30, 3, v19
	v_mul_lo_u32 v23, v30, s16
	v_add_u32_e32 v19, s24, v30
	v_add3_u32 v31, s25, v22, v23
	v_cmp_gt_u32_e64 s[14:15], s17, v22
	v_cmp_gt_u32_e32 vcc, 64, v19
	s_and_b64 s[18:19], s[14:15], vcc
	v_cmp_gt_u32_e64 s[16:17], 64, v31
	s_and_b64 s[22:23], s[18:19], s[16:17]
	v_mov_b64_e32 v[22:23], s[30:31]
	s_and_saveexec_b64 s[18:19], s[22:23]
	s_lshl_b32 s22, s40, 15
	v_lshlrev_b32_e32 v19, 6, v19
	v_or3_b32 v22, v19, s22, v31
	v_ashrrev_i32_e32 v23, 31, v22
	v_lshlrev_b64 v[22:23], 7, v[22:23]
	v_lshl_add_u64 v[22:23], s[36:37], 0, v[22:23]
	v_mov_b32_e32 v19, 0
	v_lshl_add_u64 v[22:23], v[22:23], 0, v[18:19]
	s_or_b64 exec, exec, s[18:19]
	s_lshl_b32 s46, s21, 10
	v_or_b32_e32 v19, s46, v120
	s_add_i32 s28, s52, 32
	v_readfirstlane_b32 s18, v19
	s_mov_b32 m0, s18
	s_movk_i32 s18, 0xffde
	v_mov_b64_e32 v[190:191], v[22:23]
	global_load_lds_dwordx4 v[22:23], off
	v_lshl_or_b32 v22, s28, 3, v29
	v_mul_hi_u32 v19, v22, s20
	v_lshrrev_b32_e32 v32, 3, v19
	v_mul_lo_u32 v23, v32, s18
	v_add_u32_e32 v19, s24, v32
	s_movk_i32 s18, 0x154
	v_add3_u32 v33, s25, v22, v23
	v_cmp_gt_u32_e64 s[18:19], s18, v22
	v_cmp_gt_u32_e32 vcc, 64, v19
	s_and_b64 s[22:23], s[18:19], vcc
	v_cmp_gt_u32_e64 s[20:21], 64, v33
	s_and_b64 s[22:23], s[22:23], s[20:21]
	s_xor_b64 s[22:23], s[22:23], -1
	s_and_saveexec_b64 s[34:35], s[22:23]
	s_xor_b64 s[22:23], exec, s[34:35]
	s_lshl_b32 s29, s40, 15
	s_or_saveexec_b64 s[22:23], s[22:23]
	v_mov_b32_e32 v34, s29
	v_mov_b64_e32 v[22:23], s[30:31]
	s_xor_b64 exec, exec, s[22:23]
	s_lshl_b32 s29, s40, 15
	v_lshlrev_b32_e32 v19, 6, v19
	v_or3_b32 v22, v19, s29, v33
	v_ashrrev_i32_e32 v23, 31, v22
	v_lshlrev_b64 v[22:23], 7, v[22:23]
	v_lshl_add_u64 v[22:23], s[36:37], 0, v[22:23]
	v_mov_b32_e32 v19, 0
	v_lshl_add_u64 v[22:23], v[22:23], 0, v[18:19]
	v_mov_b32_e32 v34, s29
	s_or_b64 exec, exec, s[22:23]
	s_lshl_b32 s47, s28, 10
	v_or_b32_e32 v18, s47, v120
	s_add_i32 s39, s52, 40
	v_readfirstlane_b32 s22, v18
	s_mov_b32 m0, s22
	v_lshl_or_b32 v18, s39, 3, v29
	v_mov_b64_e32 v[192:193], v[22:23]
	global_load_lds_dwordx4 v[22:23], off
	s_mov_b32 s22, 0x3c3c3c3d
	v_mul_hi_u32 v19, v18, s22
	v_lshrrev_b32_e32 v22, 3, v19
	s_movk_i32 s22, 0xffde
	s_load_dwordx2 s[34:35], s[0:1], 0x8
	v_mul_lo_u32 v19, v22, s22
	v_add_u32_e32 v35, s24, v22
	s_movk_i32 s22, 0x154
	v_add3_u32 v23, s25, v18, v19
	v_cmp_gt_u32_e64 s[22:23], s22, v18
	v_cmp_gt_u32_e32 vcc, 64, v35
	s_and_b64 s[28:29], s[22:23], vcc
	v_cmp_gt_u32_e64 s[24:25], 64, v23
	s_and_b64 s[28:29], s[28:29], s[24:25]
	s_xor_b64 s[28:29], s[28:29], -1
	s_and_saveexec_b64 s[48:49], s[28:29]
	s_xor_b64 s[28:29], exec, s[48:49]
	s_or_saveexec_b64 s[28:29], s[28:29]
	v_mov_b64_e32 v[18:19], s[30:31]
	s_xor_b64 exec, exec, s[28:29]
	v_lshlrev_b32_e32 v18, 6, v35
	v_or3_b32 v18, v18, v34, v23
	v_ashrrev_i32_e32 v19, 31, v18
	v_lshlrev_b64 v[18:19], 7, v[18:19]
	v_lshl_add_u64 v[18:19], s[36:37], 0, v[18:19]
	v_lshlrev_b32_e32 v36, 1, v20
	v_mov_b32_e32 v37, 0
	v_lshl_add_u64 v[18:19], v[18:19], 0, v[36:37]
	s_or_b64 exec, exec, s[28:29]
	v_lshrrev_b32_e32 v122, 4, v1
	v_bitop3_b32 v35, v122, v0, 6 bitop3:0x78
	s_and_b32 s48, s52, 3
	v_lshl_or_b32 v29, v29, 6, s43
	s_movk_i32 s50, 0xdc0
	v_and_b32_e32 v121, 15, v0
	v_lshlrev_b32_e32 v35, 4, v35
	s_lshr_b32 s49, s42, 8
	v_and_or_b32 v29, v29, s50, v20
	s_mul_i32 s50, s48, 0x44
	v_lshl_or_b32 v35, v121, 7, v35
	v_add_u32_e32 v123, s50, v121
	v_lshl_or_b32 v35, s49, 13, v35
	s_lshl_b32 s50, s39, 10
	s_lshl_b32 s41, s38, 6
	v_add_u32_e32 v125, 0x18000, v35
	v_or_b32_e32 v35, s50, v120
	s_lshl_b32 s38, s38, 13
	v_readfirstlane_b32 s39, v35
	s_waitcnt lgkmcnt(0)
	s_add_u32 s38, s34, s38
	s_mul_hi_u32 s57, s42, 0x38e38e39
	s_mov_b32 m0, s39
	s_addc_u32 s39, s35, 0
	s_lshr_b32 s34, s57, 12
	s_mulk_i32 s34, 0xffc1
	s_add_i32 s34, s34, s49
	s_mul_i32 s34, s49, 3
	s_lshl_b32 s56, s52, 11
	s_ashr_i32 s35, s34, 31
	s_add_i32 s52, s56, 0x18000
	s_lshl_b64 s[34:35], s[34:35], 15
	s_add_u32 s34, s38, s34
	s_addc_u32 s35, s39, s35
	s_mul_i32 s54, s49, -5
	s_add_i32 s54, s54, 6
	s_mul_hi_u32 s55, s54, 0x38e38e4
	s_mulk_i32 s55, 0xffc1
	s_add_i32 s54, s55, s54
	v_mov_b64_e32 v[194:195], v[18:19]
	global_load_lds_dwordx4 v[18:19], off
	v_lshlrev_b32_e32 v18, 1, v29
	v_mov_b32_e32 v19, 0
	s_mov_b32 m0, s52
	s_ashr_i32 s55, s54, 31
	v_lshl_add_u64 v[36:37], s[34:35], 0, v[18:19]
	global_load_lds_dwordx4 v18, s[34:35]
	s_mov_b64 s[34:35], 0x400
	s_add_i32 m0, s56, 0x18400
	s_lshl_b64 s[54:55], s[54:55], 15
	v_lshl_add_u64 v[36:37], v[36:37], 0, s[34:35]
	s_add_u32 s54, s38, s54
	global_load_lds_dwordx4 v[36:37], off
	s_addc_u32 s55, s39, s55
	s_add_i32 m0, s56, 0x1c000
	v_lshl_add_u64 v[36:37], s[54:55], 0, v[18:19]
	global_load_lds_dwordx4 v18, s[54:55]
	s_mul_i32 s54, s49, 3
	s_add_i32 s54, s54, 4
	s_mul_hi_u32 s55, s54, 0x38e38e4
	s_mulk_i32 s55, 0xffc1
	s_add_i32 s54, s55, s54
	s_ashr_i32 s55, s54, 31
	s_add_i32 m0, s56, 0x1c400
	s_lshl_b64 s[54:55], s[54:55], 15
	s_add_u32 s54, s38, s54
	v_lshl_add_u64 v[36:37], v[36:37], 0, s[34:35]
	s_addc_u32 s55, s39, s55
	global_load_lds_dwordx4 v[36:37], off
	s_add_i32 m0, s56, 0x20000
	v_lshl_add_u64 v[36:37], s[54:55], 0, v[18:19]
	global_load_lds_dwordx4 v18, s[54:55]
	v_lshl_add_u64 v[36:37], v[36:37], 0, s[34:35]
	s_add_i32 m0, s56, 0x20400
	s_lshr_b32 s54, s57, 9
	global_load_lds_dwordx4 v[36:37], off
	s_mul_i32 s54, s54, -9
	s_add_i32 s54, s54, s49
	s_mul_hi_i32 s55, s54, 0x55555556
	s_lshr_b32 s56, s55, 31
	s_add_i32 s55, s55, s56
	s_mul_i32 s55, s55, 31
	s_add_i32 s55, s55, s54
	s_bitcmp1_b32 s57, 9
	s_waitcnt vmcnt(4) lgkmcnt(0)
	s_barrier
	s_cselect_b32 s54, 0xc000, 0
	ds_read_b128 v[62:65], v125
	v_add_u32_e32 v29, s55, v123
	v_add_u32_e32 v124, 34, v123
	ds_read_b128 v[58:61], v125 offset:2048
	v_bitop3_b32 v35, v29, v122, 6 bitop3:0x6c
	v_lshl_add_u32 v29, v29, 7, s54
	v_lshl_or_b32 v139, v35, 4, v29
	ds_read_b128 v[70:73], v139
	v_add_u32_e32 v29, s55, v124
	ds_read_b128 v[66:69], v139 offset:2048
	v_bitop3_b32 v35, v29, v122, 6 bitop3:0x6c
	v_lshl_add_u32 v29, v29, 7, s54
	v_lshl_or_b32 v140, v35, 4, v29
	ds_read_b128 v[82:85], v140
	s_load_dwordx2 s[28:29], s[0:1], 0x20
	ds_read_b128 v[78:81], v140 offset:2048
	ds_read_b128 v[90:93], v125 offset:4096
	ds_read_b128 v[86:89], v125 offset:6144
	v_add_u32_e32 v127, s33, v21
	v_lshlrev_b32_e32 v20, 1, v20
	v_mov_b32_e32 v21, v19
	v_xor_b32_e32 v126, 64, v125
	s_mov_b32 s51, 0
	s_mov_b32 s53, 1
	v_add_u32_e32 v128, v34, v24
	v_lshl_add_u64 v[114:115], s[36:37], 0, v[20:21]
	v_add_u32_e32 v129, s33, v25
	v_add_u32_e32 v130, v34, v26
	v_add_u32_e32 v131, s33, v27
	v_add_u32_e32 v132, v34, v28
	v_add_u32_e32 v133, s33, v30
	v_add_u32_e32 v134, v34, v31
	v_add_u32_e32 v135, s33, v32
	v_add_u32_e32 v136, v34, v33
	v_add_u32_e32 v137, s33, v22
	v_add_u32_e32 v138, v34, v23
	v_lshl_add_u64 v[116:117], s[38:39], 0, v[18:19]
	s_mov_b64 s[36:37], 0
	s_mov_b32 s38, 0
	s_mov_b32 s39, 0
	v_mov_b32_e32 v18, v19
	v_mov_b32_e32 v20, v19
	v_mov_b32_e32 v22, v19
	v_mov_b32_e32 v23, v19
	v_mov_b32_e32 v24, v19
	v_mov_b32_e32 v25, v19
	v_mov_b32_e32 v26, v19
	v_mov_b32_e32 v27, v19
	v_mov_b32_e32 v28, v19
	v_mov_b32_e32 v29, v19
	v_mov_b32_e32 v42, v19
	v_mov_b32_e32 v43, v19
	v_mov_b32_e32 v44, v19
	v_mov_b32_e32 v45, v19
	v_mov_b32_e32 v50, v19
	v_mov_b32_e32 v51, v19
	v_mov_b32_e32 v52, v19
	v_mov_b32_e32 v53, v19
	v_mov_b32_e32 v54, v19
	v_mov_b32_e32 v55, v19
	v_mov_b32_e32 v56, v19
	v_mov_b32_e32 v57, v19
	v_mov_b32_e32 v74, v19
	v_mov_b32_e32 v75, v19
	v_mov_b32_e32 v76, v19
	v_mov_b32_e32 v77, v19
	v_mov_b32_e32 v94, v19
	v_mov_b32_e32 v95, v19
	v_mov_b32_e32 v96, v19
	v_mov_b32_e32 v97, v19
	v_mov_b32_e32 v98, v19
	v_mov_b32_e32 v99, v19
	v_mov_b32_e32 v100, v19
	v_mov_b32_e32 v101, v19
	v_mov_b32_e32 v102, v19
	v_mov_b32_e32 v103, v19
	v_mov_b32_e32 v104, v19
	v_mov_b32_e32 v105, v19
	v_mov_b32_e32 v106, v19
	v_mov_b32_e32 v107, v19
	v_mov_b32_e32 v108, v19
	v_mov_b32_e32 v109, v19
	v_mov_b32_e32 v110, v19
	v_mov_b32_e32 v111, v19
	v_mov_b32_e32 v112, v19
	v_mov_b32_e32 v113, v19
	v_mov_b32_e32 v46, v19
	v_mov_b32_e32 v47, v19
	v_mov_b32_e32 v48, v19
	v_mov_b32_e32 v49, v19
	v_mov_b32_e32 v30, v19
	v_mov_b32_e32 v31, v19
	v_mov_b32_e32 v32, v19
	v_mov_b32_e32 v33, v19
	v_mov_b32_e32 v38, v19
	v_mov_b32_e32 v39, v19
	v_mov_b32_e32 v40, v19
	v_mov_b32_e32 v41, v19
	v_mov_b32_e32 v34, v19
	v_mov_b32_e32 v35, v19
	v_mov_b32_e32 v36, v19
	v_mov_b32_e32 v37, v19
	v_mov_b32_e32 v202, 0x80000
	v_cmp_ne_u64_e64 s[76:77], v[184:185], s[30:31]
	s_nop 1
	v_cndmask_b32_e64 v196, 0, v202, s[76:77]
	v_cmp_ne_u64_e64 s[76:77], v[186:187], s[30:31]
	s_nop 1
	v_cndmask_b32_e64 v197, 0, v202, s[76:77]
	v_cmp_ne_u64_e64 s[76:77], v[188:189], s[30:31]
	s_nop 1
	v_cndmask_b32_e64 v198, 0, v202, s[76:77]
	v_cmp_ne_u64_e64 s[76:77], v[190:191], s[30:31]
	s_nop 1
	v_cndmask_b32_e64 v199, 0, v202, s[76:77]
	v_cmp_ne_u64_e64 s[76:77], v[192:193], s[30:31]
	s_nop 1
	v_cndmask_b32_e64 v200, 0, v202, s[76:77]
	v_cmp_ne_u64_e64 s[76:77], v[194:195], s[30:31]
	s_nop 1
	v_cndmask_b32_e64 v201, 0, v202, s[76:77]
	s_mov_b32 s61, 0
	s_mov_b32 s78, 0
	s_mov_b32 s67, 0
	s_mov_b32 s69, 0
	s_mov_b32 s80, 0xc000
	s_lshl_b32 s81, s49, 6
	s_lshl_b32 s79, s49, 13
	v_subrev_u32_e32 v204, s79, v125
	v_xor_b32_e32 v204, s81, v204
	v_add_u32_e32 v205, 0x2000, v204
	v_mov_b32_e32 v174, v205
	v_mov_b32_e32 v182, v123
	v_bitop3_b32 v183, v182, v122, 6 bitop3:0x6c
	v_lshl_add_u32 v182, v182, 7, 0
	v_lshl_or_b32 v176, v183, 4, v182
	v_xor_b32_e32 v176, s81, v176
	v_add_u32_e32 v182, 34, v123
	v_bitop3_b32 v183, v182, v122, 6 bitop3:0x6c
	v_lshl_add_u32 v182, v182, 7, 0
	v_lshl_or_b32 v177, v183, 4, v182
	v_xor_b32_e32 v177, s81, v177
	ds_read_b128 v[62:65], v204
	ds_read_b128 v[58:61], v204 offset:2048
	ds_read_b128 v[90:93], v204 offset:4096
	ds_read_b128 v[86:89], v204 offset:6144
	ds_read_b128 v[70:73], v176
	ds_read_b128 v[66:69], v176 offset:2048
	ds_read_b128 v[82:85], v177
	ds_read_b128 v[78:81], v177 offset:2048
	s_waitcnt lgkmcnt(0)

.Lc4_bar_0:
	s_barrier
	s_waitcnt lgkmcnt(5)
	v_mfma_f32_16x16x32_f16 v[110:113], v[62:65], v[70:73], v[110:113]
	ds_read_b128 v[142:145], v174
	s_mul_i32 s79, s49, 3
	s_add_i32 s79, s79, 2
	s_add_i32 s79, s79, s78
	s_lshl_b32 s68, s79, 15
	s_waitcnt lgkmcnt(5)
	v_mfma_f32_16x16x32_f16 v[106:109], v[58:61], v[70:73], v[106:109]
	v_add_u32_e32 v182, 68, v123
	v_bitop3_b32 v183, v182, v122, 6 bitop3:0x6c
	v_lshl_add_u32 v182, v182, 7, 0
	v_mfma_f32_16x16x32_f16 v[94:97], v[62:65], v[66:69], v[94:97]
	ds_read_b128 v[146:149], v174 offset:2048
	v_lshl_add_u64 v[178:179], v[116:117], 0, s[68:69]
	s_add_i32 s70, s38, 0xc000
	s_and_b32 s70, s70, 0xc000
	s_add_i32 s70, s70, s52
	v_mfma_f32_16x16x32_f16 v[74:77], v[58:61], v[66:69], v[74:77]
	v_lshl_or_b32 v176, v183, 4, v182
	v_xor_b32_e32 v176, s81, v176
	s_waitcnt lgkmcnt(5)
	v_mfma_f32_16x16x32_f16 v[42:45], v[62:65], v[82:85], v[42:45]
	ds_read_b128 v[150:153], v176
	v_mfma_f32_16x16x32_f16 v[26:29], v[58:61], v[82:85], v[26:29]
	v_add_u32_e32 v182, 102, v123
	v_bitop3_b32 v183, v182, v122, 6 bitop3:0x6c
	v_lshl_add_u32 v182, v182, 7, 0
	s_waitcnt lgkmcnt(5)
	v_mfma_f32_16x16x32_f16 v[46:49], v[62:65], v[78:81], v[46:49]
	ds_read_b128 v[154:157], v176 offset:2048
	v_mfma_f32_16x16x32_f16 v[30:33], v[58:61], v[78:81], v[30:33]
	v_lshl_or_b32 v177, v183, 4, v182
	v_xor_b32_e32 v177, s81, v177
	s_mov_b32 m0, s70
	s_add_i32 s71, s38, 0x4000
	global_load_lds_dwordx4 v[178:179], off
	s_waitcnt lgkmcnt(5)
	v_mfma_f32_16x16x32_f16 v[102:105], v[90:93], v[70:73], v[102:105]
	ds_read_b128 v[158:161], v177
	s_waitcnt lgkmcnt(5)
	v_mfma_f32_16x16x32_f16 v[98:101], v[86:89], v[70:73], v[98:101]
	s_and_b32 s71, s71, 0xc000
	s_add_i32 s72, s70, 0x400
	v_lshl_add_u64 v[180:181], v[178:179], 0, s[34:35]
	v_mfma_f32_16x16x32_f16 v[54:57], v[90:93], v[66:69], v[54:57]
	ds_read_b128 v[162:165], v177 offset:2048
	v_mfma_f32_16x16x32_f16 v[50:53], v[86:89], v[66:69], v[50:53]
	v_add_u32_e32 v175, s71, v204
	v_mfma_f32_16x16x32_f16 v[22:25], v[90:93], v[82:85], v[22:25]
	ds_read_b128 v[166:169], v174 offset:4096
	v_mfma_f32_16x16x32_f16 v[18:21], v[86:89], v[82:85], v[18:21]
	v_mfma_f32_16x16x32_f16 v[38:41], v[90:93], v[78:81], v[38:41]
	ds_read_b128 v[170:173], v174 offset:6144
	v_mfma_f32_16x16x32_f16 v[34:37], v[86:89], v[78:81], v[34:37]
	v_add_u32_e32 v174, s71, v205
	s_waitcnt lgkmcnt(7)
	v_mfma_f32_16x16x32_f16 v[110:113], v[142:145], v[82:85], v[110:113]
	ds_read_b128 v[62:65], v175
	s_waitcnt lgkmcnt(7)
	v_mfma_f32_16x16x32_f16 v[106:109], v[146:149], v[82:85], v[106:109]
	v_add_u32_e32 v182, 1, v123
	v_bitop3_b32 v183, v182, v122, 6 bitop3:0x6c
	v_lshl_add_u32 v182, v182, 7, 0
	v_mfma_f32_16x16x32_f16 v[94:97], v[142:145], v[78:81], v[94:97]
	ds_read_b128 v[58:61], v175 offset:2048
	v_mfma_f32_16x16x32_f16 v[74:77], v[146:149], v[78:81], v[74:77]
	v_lshl_or_b32 v176, v183, 4, v182
	v_xor_b32_e32 v176, s81, v176
	s_waitcnt lgkmcnt(7)
	v_mfma_f32_16x16x32_f16 v[42:45], v[142:145], v[150:153], v[42:45]
	ds_read_b128 v[70:73], v176
	v_mfma_f32_16x16x32_f16 v[26:29], v[146:149], v[150:153], v[26:29]
	s_waitcnt lgkmcnt(7)
	v_mfma_f32_16x16x32_f16 v[46:49], v[142:145], v[154:157], v[46:49]
	ds_read_b128 v[66:69], v176 offset:2048
	v_mfma_f32_16x16x32_f16 v[30:33], v[146:149], v[154:157], v[30:33]
	s_mov_b32 m0, s72
	s_addk_i32 s38, 0x4000
	global_load_lds_dwordx4 v[180:181], off
	s_waitcnt lgkmcnt(5)
	v_mfma_f32_16x16x32_f16 v[102:105], v[166:169], v[82:85], v[102:105]
	s_waitcnt lgkmcnt(4)
	v_mfma_f32_16x16x32_f16 v[98:101], v[170:173], v[82:85], v[98:101]
	v_mfma_f32_16x16x32_f16 v[54:57], v[166:169], v[78:81], v[54:57]
	v_mfma_f32_16x16x32_f16 v[50:53], v[170:173], v[78:81], v[50:53]
	v_mfma_f32_16x16x32_f16 v[22:25], v[166:169], v[150:153], v[22:25]
	ds_read_b128 v[90:93], v175 offset:4096
	v_mfma_f32_16x16x32_f16 v[18:21], v[170:173], v[150:153], v[18:21]
	v_mfma_f32_16x16x32_f16 v[38:41], v[166:169], v[154:157], v[38:41]
	ds_read_b128 v[86:89], v175 offset:6144
	v_mfma_f32_16x16x32_f16 v[34:37], v[170:173], v[154:157], v[34:37]
	s_cmp_gt_u32 s53, 7
	s_cbranch_scc1 .Lc4_np0
	s_bitcmp1_b32 s53, 0
	s_cselect_b32 s56, 0xc000, 0
	s_add_i32 m0, s56, s43
	v_mad_u64_u32 v[118:119], s[76:77], v196, s53, v[184:185]
	global_load_lds_dwordx4 v[118:119], off
	s_add_i32 m0, s56, s44
	v_mad_u64_u32 v[118:119], s[76:77], v197, s53, v[186:187]
	global_load_lds_dwordx4 v[118:119], off
	s_add_i32 m0, s56, s45
	v_mad_u64_u32 v[118:119], s[76:77], v198, s53, v[188:189]
	global_load_lds_dwordx4 v[118:119], off
	s_add_i32 m0, s56, s46
	v_mad_u64_u32 v[118:119], s[76:77], v199, s53, v[190:191]
	global_load_lds_dwordx4 v[118:119], off
	s_add_i32 m0, s56, s47
	v_mad_u64_u32 v[118:119], s[76:77], v200, s53, v[192:193]
	global_load_lds_dwordx4 v[118:119], off
	s_add_i32 m0, s56, s50
	v_mad_u64_u32 v[118:119], s[76:77], v201, s53, v[194:195]
	global_load_lds_dwordx4 v[118:119], off
	s_add_i32 s53, s53, 1
	s_mov_b32 s67, 2

.Lc4_bar_1:
	s_barrier
	s_waitcnt lgkmcnt(5)
	v_mfma_f32_16x16x32_f16 v[110:113], v[62:65], v[150:153], v[110:113]
	ds_read_b128 v[142:145], v174
	s_mul_i32 s79, s49, 1
	s_add_i32 s79, s79, 8
	s_add_i32 s79, s79, s78
	s_lshl_b32 s68, s79, 15
	s_waitcnt lgkmcnt(5)
	v_mfma_f32_16x16x32_f16 v[106:109], v[58:61], v[150:153], v[106:109]
	v_add_u32_e32 v182, 35, v123
	v_bitop3_b32 v183, v182, v122, 6 bitop3:0x6c
	v_lshl_add_u32 v182, v182, 7, 0
	v_mfma_f32_16x16x32_f16 v[94:97], v[62:65], v[154:157], v[94:97]
	ds_read_b128 v[146:149], v174 offset:2048
	v_lshl_add_u64 v[178:179], v[116:117], 0, s[68:69]
	s_add_i32 s70, s38, 0xc000
	s_and_b32 s70, s70, 0xc000
	s_add_i32 s70, s70, s52
	v_mfma_f32_16x16x32_f16 v[74:77], v[58:61], v[154:157], v[74:77]
	v_lshl_or_b32 v176, v183, 4, v182
	v_xor_b32_e32 v176, s81, v176
	v_mfma_f32_16x16x32_f16 v[42:45], v[62:65], v[158:161], v[42:45]
	ds_read_b128 v[82:85], v176
	v_mfma_f32_16x16x32_f16 v[26:29], v[58:61], v[158:161], v[26:29]
	v_mfma_f32_16x16x32_f16 v[46:49], v[62:65], v[162:165], v[46:49]
	ds_read_b128 v[78:81], v176 offset:2048
	v_mfma_f32_16x16x32_f16 v[30:33], v[58:61], v[162:165], v[30:33]
	s_mov_b32 m0, s70
	s_add_i32 s71, s38, 0x4000
	global_load_lds_dwordx4 v[178:179], off
	s_waitcnt lgkmcnt(5)
	v_mfma_f32_16x16x32_f16 v[102:105], v[90:93], v[150:153], v[102:105]
	s_waitcnt lgkmcnt(4)
	v_mfma_f32_16x16x32_f16 v[98:101], v[86:89], v[150:153], v[98:101]
	s_and_b32 s71, s71, 0xc000
	s_add_i32 s72, s70, 0x400
	v_lshl_add_u64 v[180:181], v[178:179], 0, s[34:35]
	v_mfma_f32_16x16x32_f16 v[54:57], v[90:93], v[154:157], v[54:57]
	v_mfma_f32_16x16x32_f16 v[50:53], v[86:89], v[154:157], v[50:53]
	v_add_u32_e32 v175, s71, v204
	v_mfma_f32_16x16x32_f16 v[22:25], v[90:93], v[158:161], v[22:25]
	ds_read_b128 v[166:169], v174 offset:4096
	v_mfma_f32_16x16x32_f16 v[18:21], v[86:89], v[158:161], v[18:21]
	v_mfma_f32_16x16x32_f16 v[38:41], v[90:93], v[162:165], v[38:41]
	ds_read_b128 v[170:173], v174 offset:6144
	v_mfma_f32_16x16x32_f16 v[34:37], v[86:89], v[162:165], v[34:37]
	v_add_u32_e32 v174, s71, v205
	s_waitcnt lgkmcnt(5)
	v_mfma_f32_16x16x32_f16 v[110:113], v[142:145], v[70:73], v[110:113]
	ds_read_b128 v[62:65], v175
	s_waitcnt lgkmcnt(5)
	v_mfma_f32_16x16x32_f16 v[106:109], v[146:149], v[70:73], v[106:109]
	v_add_u32_e32 v182, 69, v123
	v_bitop3_b32 v183, v182, v122, 6 bitop3:0x6c
	v_lshl_add_u32 v182, v182, 7, 0
	v_mfma_f32_16x16x32_f16 v[94:97], v[142:145], v[66:69], v[94:97]
	ds_read_b128 v[58:61], v175 offset:2048
	v_mfma_f32_16x16x32_f16 v[74:77], v[146:149], v[66:69], v[74:77]
	v_lshl_or_b32 v176, v183, 4, v182
	v_xor_b32_e32 v176, s81, v176
	s_waitcnt lgkmcnt(5)
	v_mfma_f32_16x16x32_f16 v[42:45], v[142:145], v[82:85], v[42:45]
	ds_read_b128 v[150:153], v176
	v_mfma_f32_16x16x32_f16 v[26:29], v[146:149], v[82:85], v[26:29]
	v_add_u32_e32 v182, 103, v123
	v_bitop3_b32 v183, v182, v122, 6 bitop3:0x6c
	v_lshl_add_u32 v182, v182, 7, 0
	s_waitcnt lgkmcnt(5)
	v_mfma_f32_16x16x32_f16 v[46:49], v[142:145], v[78:81], v[46:49]
	ds_read_b128 v[154:157], v176 offset:2048
	v_mfma_f32_16x16x32_f16 v[30:33], v[146:149], v[78:81], v[30:33]
	v_lshl_or_b32 v177, v183, 4, v182
	v_xor_b32_e32 v177, s81, v177
	s_mov_b32 m0, s72
	s_addk_i32 s38, 0x4000
	global_load_lds_dwordx4 v[180:181], off
	s_waitcnt lgkmcnt(5)
	v_mfma_f32_16x16x32_f16 v[102:105], v[166:169], v[70:73], v[102:105]
	ds_read_b128 v[158:161], v177
	s_waitcnt lgkmcnt(5)
	v_mfma_f32_16x16x32_f16 v[98:101], v[170:173], v[70:73], v[98:101]
	v_mfma_f32_16x16x32_f16 v[54:57], v[166:169], v[66:69], v[54:57]
	ds_read_b128 v[162:165], v177 offset:2048
	v_mfma_f32_16x16x32_f16 v[50:53], v[170:173], v[66:69], v[50:53]
	v_mfma_f32_16x16x32_f16 v[22:25], v[166:169], v[82:85], v[22:25]
	ds_read_b128 v[90:93], v175 offset:4096
	v_mfma_f32_16x16x32_f16 v[18:21], v[170:173], v[82:85], v[18:21]
	v_mfma_f32_16x16x32_f16 v[38:41], v[166:169], v[78:81], v[38:41]
	ds_read_b128 v[86:89], v175 offset:6144
	v_mfma_f32_16x16x32_f16 v[34:37], v[170:173], v[78:81], v[34:37]
	s_cmp_eq_u32 s67, 0
	s_cbranch_scc1 .Lc4_w2_2
	s_waitcnt vmcnt(8)
	s_sub_i32 s67, s67, 1
	s_branch .Lc4_bar_2

.Lc4_bar_2:
	s_barrier
	s_waitcnt lgkmcnt(7)
	v_mfma_f32_16x16x32_f16 v[110:113], v[62:65], v[82:85], v[110:113]
	ds_read_b128 v[142:145], v174
	s_mul_i32 s79, s49, 3
	s_add_i32 s79, s79, 12
	s_add_i32 s79, s79, s78
	s_lshl_b32 s68, s79, 15
	s_waitcnt lgkmcnt(7)
	v_mfma_f32_16x16x32_f16 v[106:109], v[58:61], v[82:85], v[106:109]
	v_add_u32_e32 v182, 2, v123
	v_bitop3_b32 v183, v182, v122, 6 bitop3:0x6c
	v_lshl_add_u32 v182, v182, 7, 0
	v_mfma_f32_16x16x32_f16 v[94:97], v[62:65], v[78:81], v[94:97]
	ds_read_b128 v[146:149], v174 offset:2048
	v_lshl_add_u64 v[178:179], v[116:117], 0, s[68:69]
	s_add_i32 s70, s38, 0xc000
	s_and_b32 s70, s70, 0xc000
	s_add_i32 s70, s70, s52
	v_mfma_f32_16x16x32_f16 v[74:77], v[58:61], v[78:81], v[74:77]
	v_lshl_or_b32 v176, v183, 4, v182
	v_xor_b32_e32 v176, s81, v176
	s_waitcnt lgkmcnt(7)
	v_mfma_f32_16x16x32_f16 v[42:45], v[62:65], v[150:153], v[42:45]
	ds_read_b128 v[70:73], v176
	v_mfma_f32_16x16x32_f16 v[26:29], v[58:61], v[150:153], v[26:29]
	s_waitcnt lgkmcnt(7)
	v_mfma_f32_16x16x32_f16 v[46:49], v[62:65], v[154:157], v[46:49]
	ds_read_b128 v[66:69], v176 offset:2048
	v_mfma_f32_16x16x32_f16 v[30:33], v[58:61], v[154:157], v[30:33]
	s_mov_b32 m0, s70
	s_add_i32 s71, s38, 0x4000
	global_load_lds_dwordx4 v[178:179], off
	s_waitcnt lgkmcnt(5)
	v_mfma_f32_16x16x32_f16 v[102:105], v[90:93], v[82:85], v[102:105]
	s_waitcnt lgkmcnt(4)
	v_mfma_f32_16x16x32_f16 v[98:101], v[86:89], v[82:85], v[98:101]
	s_and_b32 s71, s71, 0xc000
	s_add_i32 s72, s70, 0x400
	v_lshl_add_u64 v[180:181], v[178:179], 0, s[34:35]
	v_mfma_f32_16x16x32_f16 v[54:57], v[90:93], v[78:81], v[54:57]
	v_mfma_f32_16x16x32_f16 v[50:53], v[86:89], v[78:81], v[50:53]
	v_add_u32_e32 v175, s71, v204
	v_mfma_f32_16x16x32_f16 v[22:25], v[90:93], v[150:153], v[22:25]
	ds_read_b128 v[166:169], v174 offset:4096
	v_mfma_f32_16x16x32_f16 v[18:21], v[86:89], v[150:153], v[18:21]
	v_mfma_f32_16x16x32_f16 v[38:41], v[90:93], v[154:157], v[38:41]
	ds_read_b128 v[170:173], v174 offset:6144
	v_mfma_f32_16x16x32_f16 v[34:37], v[86:89], v[154:157], v[34:37]
	v_add_u32_e32 v174, s71, v205
	s_waitcnt lgkmcnt(5)
	v_mfma_f32_16x16x32_f16 v[110:113], v[142:145], v[150:153], v[110:113]
	ds_read_b128 v[62:65], v175
	s_waitcnt lgkmcnt(5)
	v_mfma_f32_16x16x32_f16 v[106:109], v[146:149], v[150:153], v[106:109]
	v_add_u32_e32 v182, 36, v123
	v_bitop3_b32 v183, v182, v122, 6 bitop3:0x6c
	v_lshl_add_u32 v182, v182, 7, 0
	v_mfma_f32_16x16x32_f16 v[94:97], v[142:145], v[154:157], v[94:97]
	ds_read_b128 v[58:61], v175 offset:2048
	v_mfma_f32_16x16x32_f16 v[74:77], v[146:149], v[154:157], v[74:77]
	v_lshl_or_b32 v176, v183, 4, v182
	v_xor_b32_e32 v176, s81, v176
	v_mfma_f32_16x16x32_f16 v[42:45], v[142:145], v[158:161], v[42:45]
	ds_read_b128 v[82:85], v176
	v_mfma_f32_16x16x32_f16 v[26:29], v[146:149], v[158:161], v[26:29]
	v_mfma_f32_16x16x32_f16 v[46:49], v[142:145], v[162:165], v[46:49]
	ds_read_b128 v[78:81], v176 offset:2048
	v_mfma_f32_16x16x32_f16 v[30:33], v[146:149], v[162:165], v[30:33]
	s_mov_b32 m0, s72
	s_addk_i32 s38, 0x4000
	global_load_lds_dwordx4 v[180:181], off
	s_waitcnt lgkmcnt(5)
	v_mfma_f32_16x16x32_f16 v[102:105], v[166:169], v[150:153], v[102:105]
	s_waitcnt lgkmcnt(4)
	v_mfma_f32_16x16x32_f16 v[98:101], v[170:173], v[150:153], v[98:101]
	v_mfma_f32_16x16x32_f16 v[54:57], v[166:169], v[154:157], v[54:57]
	v_mfma_f32_16x16x32_f16 v[50:53], v[170:173], v[154:157], v[50:53]
	v_mfma_f32_16x16x32_f16 v[22:25], v[166:169], v[158:161], v[22:25]
	ds_read_b128 v[90:93], v175 offset:4096
	v_mfma_f32_16x16x32_f16 v[18:21], v[170:173], v[158:161], v[18:21]
	v_mfma_f32_16x16x32_f16 v[38:41], v[166:169], v[162:165], v[38:41]
	ds_read_b128 v[86:89], v175 offset:6144
	v_mfma_f32_16x16x32_f16 v[34:37], v[170:173], v[162:165], v[34:37]
	s_cmp_eq_u32 s67, 0
	s_cbranch_scc1 .Lc4_w2_3
	s_waitcnt vmcnt(8)
	s_sub_i32 s67, s67, 1
	s_branch .Lc4_bar_3

.Lc4_bar_3:
	s_barrier
	s_waitcnt lgkmcnt(5)
	v_mfma_f32_16x16x32_f16 v[110:113], v[62:65], v[70:73], v[110:113]
	ds_read_b128 v[142:145], v174
	s_mul_i32 s79, s49, 3
	s_add_i32 s79, s79, 10
	s_add_i32 s79, s79, s78
	s_lshl_b32 s68, s79, 15
	s_waitcnt lgkmcnt(5)
	v_mfma_f32_16x16x32_f16 v[106:109], v[58:61], v[70:73], v[106:109]
	v_add_u32_e32 v182, 70, v123
	v_bitop3_b32 v183, v182, v122, 6 bitop3:0x6c
	v_lshl_add_u32 v182, v182, 7, 0
	v_mfma_f32_16x16x32_f16 v[94:97], v[62:65], v[66:69], v[94:97]
	ds_read_b128 v[146:149], v174 offset:2048
	v_lshl_add_u64 v[178:179], v[116:117], 0, s[68:69]
	s_add_i32 s70, s38, 0xc000
	s_and_b32 s70, s70, 0xc000
	s_add_i32 s70, s70, s52
	v_mfma_f32_16x16x32_f16 v[74:77], v[58:61], v[66:69], v[74:77]
	v_lshl_or_b32 v176, v183, 4, v182
	v_xor_b32_e32 v176, s81, v176
	s_waitcnt lgkmcnt(5)
	v_mfma_f32_16x16x32_f16 v[42:45], v[62:65], v[82:85], v[42:45]
	ds_read_b128 v[150:153], v176
	v_mfma_f32_16x16x32_f16 v[26:29], v[58:61], v[82:85], v[26:29]
	v_add_u32_e32 v182, 104, v123
	v_bitop3_b32 v183, v182, v122, 6 bitop3:0x6c
	v_lshl_add_u32 v182, v182, 7, 0
	s_waitcnt lgkmcnt(5)
	v_mfma_f32_16x16x32_f16 v[46:49], v[62:65], v[78:81], v[46:49]
	ds_read_b128 v[154:157], v176 offset:2048
	v_mfma_f32_16x16x32_f16 v[30:33], v[58:61], v[78:81], v[30:33]
	v_lshl_or_b32 v177, v183, 4, v182
	v_xor_b32_e32 v177, s81, v177
	s_mov_b32 m0, s70
	s_add_i32 s71, s38, 0x4000
	global_load_lds_dwordx4 v[178:179], off
	s_waitcnt lgkmcnt(5)
	v_mfma_f32_16x16x32_f16 v[102:105], v[90:93], v[70:73], v[102:105]
	ds_read_b128 v[158:161], v177
	s_waitcnt lgkmcnt(5)
	v_mfma_f32_16x16x32_f16 v[98:101], v[86:89], v[70:73], v[98:101]
	s_and_b32 s71, s71, 0xc000
	s_add_i32 s72, s70, 0x400
	v_lshl_add_u64 v[180:181], v[178:179], 0, s[34:35]
	v_mfma_f32_16x16x32_f16 v[54:57], v[90:93], v[66:69], v[54:57]
	ds_read_b128 v[162:165], v177 offset:2048
	v_mfma_f32_16x16x32_f16 v[50:53], v[86:89], v[66:69], v[50:53]
	v_add_u32_e32 v175, s71, v204
	v_mfma_f32_16x16x32_f16 v[22:25], v[90:93], v[82:85], v[22:25]
	ds_read_b128 v[166:169], v174 offset:4096
	v_mfma_f32_16x16x32_f16 v[18:21], v[86:89], v[82:85], v[18:21]
	v_mfma_f32_16x16x32_f16 v[38:41], v[90:93], v[78:81], v[38:41]
	ds_read_b128 v[170:173], v174 offset:6144
	v_mfma_f32_16x16x32_f16 v[34:37], v[86:89], v[78:81], v[34:37]
	v_add_u32_e32 v174, s71, v205
	s_waitcnt lgkmcnt(7)
	v_mfma_f32_16x16x32_f16 v[110:113], v[142:145], v[82:85], v[110:113]
	ds_read_b128 v[62:65], v175
	s_waitcnt lgkmcnt(7)
	v_mfma_f32_16x16x32_f16 v[106:109], v[146:149], v[82:85], v[106:109]
	v_mov_b32_e32 v182, v123
	v_bitop3_b32 v183, v182, v122, 6 bitop3:0x6c
	v_lshl_add_u32 v182, v182, 7, s80
	v_mfma_f32_16x16x32_f16 v[94:97], v[142:145], v[78:81], v[94:97]
	ds_read_b128 v[58:61], v175 offset:2048
	v_mfma_f32_16x16x32_f16 v[74:77], v[146:149], v[78:81], v[74:77]
	v_lshl_or_b32 v176, v183, 4, v182
	v_xor_b32_e32 v176, s81, v176
	s_waitcnt lgkmcnt(7)
	v_mfma_f32_16x16x32_f16 v[42:45], v[142:145], v[150:153], v[42:45]
	ds_read_b128 v[70:73], v176
	v_mfma_f32_16x16x32_f16 v[26:29], v[146:149], v[150:153], v[26:29]
	s_waitcnt lgkmcnt(7)
	v_mfma_f32_16x16x32_f16 v[46:49], v[142:145], v[154:157], v[46:49]
	ds_read_b128 v[66:69], v176 offset:2048
	v_mfma_f32_16x16x32_f16 v[30:33], v[146:149], v[154:157], v[30:33]
	s_mov_b32 m0, s72
	s_addk_i32 s38, 0x4000
	global_load_lds_dwordx4 v[180:181], off
	s_waitcnt lgkmcnt(5)
	v_mfma_f32_16x16x32_f16 v[102:105], v[166:169], v[82:85], v[102:105]
	s_waitcnt lgkmcnt(4)
	v_mfma_f32_16x16x32_f16 v[98:101], v[170:173], v[82:85], v[98:101]
	v_mfma_f32_16x16x32_f16 v[54:57], v[166:169], v[78:81], v[54:57]
	v_mfma_f32_16x16x32_f16 v[50:53], v[170:173], v[78:81], v[50:53]
	v_mfma_f32_16x16x32_f16 v[22:25], v[166:169], v[150:153], v[22:25]
	ds_read_b128 v[90:93], v175 offset:4096
	v_mfma_f32_16x16x32_f16 v[18:21], v[170:173], v[150:153], v[18:21]
	v_mfma_f32_16x16x32_f16 v[38:41], v[166:169], v[154:157], v[38:41]
	ds_read_b128 v[86:89], v175 offset:6144
	v_mfma_f32_16x16x32_f16 v[34:37], v[170:173], v[154:157], v[34:37]
	s_cmp_eq_u32 s67, 0
	s_cbranch_scc1 .Lc4_w2_4
	s_waitcnt vmcnt(8)
	s_sub_i32 s67, s67, 1
	s_branch .Lc4_bar_4

.Lc4_bar_4:
	s_barrier
	s_waitcnt lgkmcnt(5)
	v_mfma_f32_16x16x32_f16 v[110:113], v[62:65], v[150:153], v[110:113]
	ds_read_b128 v[142:145], v174
	s_mul_i32 s79, s49, -5
	s_add_i32 s79, s79, 16
	s_add_i32 s79, s79, s78
	s_lshl_b32 s68, s79, 15
	s_waitcnt lgkmcnt(5)
	v_mfma_f32_16x16x32_f16 v[106:109], v[58:61], v[150:153], v[106:109]
	v_add_u32_e32 v182, 34, v123
	v_bitop3_b32 v183, v182, v122, 6 bitop3:0x6c
	v_lshl_add_u32 v182, v182, 7, s80
	v_mfma_f32_16x16x32_f16 v[94:97], v[62:65], v[154:157], v[94:97]
	ds_read_b128 v[146:149], v174 offset:2048
	v_lshl_add_u64 v[178:179], v[116:117], 0, s[68:69]
	s_add_i32 s70, s38, 0xc000
	s_and_b32 s70, s70, 0xc000
	s_add_i32 s70, s70, s52
	v_mfma_f32_16x16x32_f16 v[74:77], v[58:61], v[154:157], v[74:77]
	v_lshl_or_b32 v176, v183, 4, v182
	v_xor_b32_e32 v176, s81, v176
	v_mfma_f32_16x16x32_f16 v[42:45], v[62:65], v[158:161], v[42:45]
	ds_read_b128 v[82:85], v176
	v_mfma_f32_16x16x32_f16 v[26:29], v[58:61], v[158:161], v[26:29]
	v_mfma_f32_16x16x32_f16 v[46:49], v[62:65], v[162:165], v[46:49]
	ds_read_b128 v[78:81], v176 offset:2048
	v_mfma_f32_16x16x32_f16 v[30:33], v[58:61], v[162:165], v[30:33]
	s_mov_b32 m0, s70
	s_add_i32 s71, s38, 0x4000
	global_load_lds_dwordx4 v[178:179], off
	s_waitcnt lgkmcnt(5)
	v_mfma_f32_16x16x32_f16 v[102:105], v[90:93], v[150:153], v[102:105]
	s_waitcnt lgkmcnt(4)
	v_mfma_f32_16x16x32_f16 v[98:101], v[86:89], v[150:153], v[98:101]
	s_and_b32 s71, s71, 0xc000
	s_add_i32 s72, s70, 0x400
	v_lshl_add_u64 v[180:181], v[178:179], 0, s[34:35]
	v_mfma_f32_16x16x32_f16 v[54:57], v[90:93], v[154:157], v[54:57]
	v_mfma_f32_16x16x32_f16 v[50:53], v[86:89], v[154:157], v[50:53]
	v_add_u32_e32 v175, s71, v204
	v_mfma_f32_16x16x32_f16 v[22:25], v[90:93], v[158:161], v[22:25]
	ds_read_b128 v[166:169], v174 offset:4096
	v_mfma_f32_16x16x32_f16 v[18:21], v[86:89], v[158:161], v[18:21]
	v_mfma_f32_16x16x32_f16 v[38:41], v[90:93], v[162:165], v[38:41]
	ds_read_b128 v[170:173], v174 offset:6144
	v_mfma_f32_16x16x32_f16 v[34:37], v[86:89], v[162:165], v[34:37]
	v_add_u32_e32 v174, s71, v205
	s_waitcnt lgkmcnt(5)
	v_mfma_f32_16x16x32_f16 v[110:113], v[142:145], v[70:73], v[110:113]
	ds_read_b128 v[62:65], v175
	s_waitcnt lgkmcnt(5)
	v_mfma_f32_16x16x32_f16 v[106:109], v[146:149], v[70:73], v[106:109]
	v_add_u32_e32 v182, 68, v123
	v_bitop3_b32 v183, v182, v122, 6 bitop3:0x6c
	v_lshl_add_u32 v182, v182, 7, s80
	v_mfma_f32_16x16x32_f16 v[94:97], v[142:145], v[66:69], v[94:97]
	ds_read_b128 v[58:61], v175 offset:2048
	v_mfma_f32_16x16x32_f16 v[74:77], v[146:149], v[66:69], v[74:77]
	v_lshl_or_b32 v176, v183, 4, v182
	v_xor_b32_e32 v176, s81, v176
	s_waitcnt lgkmcnt(5)
	v_mfma_f32_16x16x32_f16 v[42:45], v[142:145], v[82:85], v[42:45]
	ds_read_b128 v[150:153], v176
	v_mfma_f32_16x16x32_f16 v[26:29], v[146:149], v[82:85], v[26:29]
	v_add_u32_e32 v182, 102, v123
	v_bitop3_b32 v183, v182, v122, 6 bitop3:0x6c
	v_lshl_add_u32 v182, v182, 7, s80
	s_waitcnt lgkmcnt(5)
	v_mfma_f32_16x16x32_f16 v[46:49], v[142:145], v[78:81], v[46:49]
	ds_read_b128 v[154:157], v176 offset:2048
	v_mfma_f32_16x16x32_f16 v[30:33], v[146:149], v[78:81], v[30:33]
	v_lshl_or_b32 v177, v183, 4, v182
	v_xor_b32_e32 v177, s81, v177
	s_mov_b32 m0, s72
	s_addk_i32 s38, 0x4000
	global_load_lds_dwordx4 v[180:181], off
	s_waitcnt lgkmcnt(5)
	v_mfma_f32_16x16x32_f16 v[102:105], v[166:169], v[70:73], v[102:105]
	ds_read_b128 v[158:161], v177
	s_waitcnt lgkmcnt(5)
	v_mfma_f32_16x16x32_f16 v[98:101], v[170:173], v[70:73], v[98:101]
	v_mfma_f32_16x16x32_f16 v[54:57], v[166:169], v[66:69], v[54:57]
	ds_read_b128 v[162:165], v177 offset:2048
	v_mfma_f32_16x16x32_f16 v[50:53], v[170:173], v[66:69], v[50:53]
	v_mfma_f32_16x16x32_f16 v[22:25], v[166:169], v[82:85], v[22:25]
	ds_read_b128 v[90:93], v175 offset:4096
	v_mfma_f32_16x16x32_f16 v[18:21], v[170:173], v[82:85], v[18:21]
	v_mfma_f32_16x16x32_f16 v[38:41], v[166:169], v[78:81], v[38:41]
	ds_read_b128 v[86:89], v175 offset:6144
	v_mfma_f32_16x16x32_f16 v[34:37], v[170:173], v[78:81], v[34:37]
	s_cmp_eq_u32 s67, 0
	s_cbranch_scc1 .Lc4_w2_5
	s_waitcnt vmcnt(8)
	s_sub_i32 s67, s67, 1
	s_branch .Lc4_bar_5

.Lc4_bar_5:
	s_barrier
	s_waitcnt lgkmcnt(7)
	v_mfma_f32_16x16x32_f16 v[110:113], v[62:65], v[82:85], v[110:113]
	ds_read_b128 v[142:145], v174
	s_mul_i32 s79, s49, 3
	s_add_i32 s79, s79, 14
	s_add_i32 s79, s79, s78
	s_lshl_b32 s68, s79, 15
	s_waitcnt lgkmcnt(7)
	v_mfma_f32_16x16x32_f16 v[106:109], v[58:61], v[82:85], v[106:109]
	v_add_u32_e32 v182, 1, v123
	v_bitop3_b32 v183, v182, v122, 6 bitop3:0x6c
	v_lshl_add_u32 v182, v182, 7, s80
	v_mfma_f32_16x16x32_f16 v[94:97], v[62:65], v[78:81], v[94:97]
	ds_read_b128 v[146:149], v174 offset:2048
	v_lshl_add_u64 v[178:179], v[116:117], 0, s[68:69]
	s_add_i32 s70, s38, 0xc000
	s_and_b32 s70, s70, 0xc000
	s_add_i32 s70, s70, s52
	v_mfma_f32_16x16x32_f16 v[74:77], v[58:61], v[78:81], v[74:77]
	v_lshl_or_b32 v176, v183, 4, v182
	v_xor_b32_e32 v176, s81, v176
	s_waitcnt lgkmcnt(7)
	v_mfma_f32_16x16x32_f16 v[42:45], v[62:65], v[150:153], v[42:45]
	ds_read_b128 v[70:73], v176
	v_mfma_f32_16x16x32_f16 v[26:29], v[58:61], v[150:153], v[26:29]
	s_waitcnt lgkmcnt(7)
	v_mfma_f32_16x16x32_f16 v[46:49], v[62:65], v[154:157], v[46:49]
	ds_read_b128 v[66:69], v176 offset:2048
	v_mfma_f32_16x16x32_f16 v[30:33], v[58:61], v[154:157], v[30:33]
	s_mov_b32 m0, s70
	s_add_i32 s71, s38, 0x4000
	global_load_lds_dwordx4 v[178:179], off
	s_waitcnt lgkmcnt(5)
	v_mfma_f32_16x16x32_f16 v[102:105], v[90:93], v[82:85], v[102:105]
	s_waitcnt lgkmcnt(4)
	v_mfma_f32_16x16x32_f16 v[98:101], v[86:89], v[82:85], v[98:101]
	s_and_b32 s71, s71, 0xc000
	s_add_i32 s72, s70, 0x400
	v_lshl_add_u64 v[180:181], v[178:179], 0, s[34:35]
	v_mfma_f32_16x16x32_f16 v[54:57], v[90:93], v[78:81], v[54:57]
	v_mfma_f32_16x16x32_f16 v[50:53], v[86:89], v[78:81], v[50:53]
	v_add_u32_e32 v175, s71, v204
	v_mfma_f32_16x16x32_f16 v[22:25], v[90:93], v[150:153], v[22:25]
	ds_read_b128 v[166:169], v174 offset:4096
	v_mfma_f32_16x16x32_f16 v[18:21], v[86:89], v[150:153], v[18:21]
	v_mfma_f32_16x16x32_f16 v[38:41], v[90:93], v[154:157], v[38:41]
	ds_read_b128 v[170:173], v174 offset:6144
	v_mfma_f32_16x16x32_f16 v[34:37], v[86:89], v[154:157], v[34:37]
	v_add_u32_e32 v174, s71, v205
	s_waitcnt lgkmcnt(5)
	v_mfma_f32_16x16x32_f16 v[110:113], v[142:145], v[150:153], v[110:113]
	ds_read_b128 v[62:65], v175
	s_waitcnt lgkmcnt(5)
	v_mfma_f32_16x16x32_f16 v[106:109], v[146:149], v[150:153], v[106:109]
	v_add_u32_e32 v182, 35, v123
	v_bitop3_b32 v183, v182, v122, 6 bitop3:0x6c
	v_lshl_add_u32 v182, v182, 7, s80
	v_mfma_f32_16x16x32_f16 v[94:97], v[142:145], v[154:157], v[94:97]
	ds_read_b128 v[58:61], v175 offset:2048
	v_mfma_f32_16x16x32_f16 v[74:77], v[146:149], v[154:157], v[74:77]
	v_lshl_or_b32 v176, v183, 4, v182
	v_xor_b32_e32 v176, s81, v176
	v_mfma_f32_16x16x32_f16 v[42:45], v[142:145], v[158:161], v[42:45]
	ds_read_b128 v[82:85], v176
	v_mfma_f32_16x16x32_f16 v[26:29], v[146:149], v[158:161], v[26:29]
	v_mfma_f32_16x16x32_f16 v[46:49], v[142:145], v[162:165], v[46:49]
	ds_read_b128 v[78:81], v176 offset:2048
	v_mfma_f32_16x16x32_f16 v[30:33], v[146:149], v[162:165], v[30:33]
	s_mov_b32 m0, s72
	s_addk_i32 s38, 0x4000
	global_load_lds_dwordx4 v[180:181], off
	s_waitcnt lgkmcnt(5)
	v_mfma_f32_16x16x32_f16 v[102:105], v[166:169], v[150:153], v[102:105]
	s_waitcnt lgkmcnt(4)
	v_mfma_f32_16x16x32_f16 v[98:101], v[170:173], v[150:153], v[98:101]
	v_mfma_f32_16x16x32_f16 v[54:57], v[166:169], v[154:157], v[54:57]
	v_mfma_f32_16x16x32_f16 v[50:53], v[170:173], v[154:157], v[50:53]
	v_mfma_f32_16x16x32_f16 v[22:25], v[166:169], v[158:161], v[22:25]
	ds_read_b128 v[90:93], v175 offset:4096
	v_mfma_f32_16x16x32_f16 v[18:21], v[170:173], v[158:161], v[18:21]
	v_mfma_f32_16x16x32_f16 v[38:41], v[166:169], v[162:165], v[38:41]
	ds_read_b128 v[86:89], v175 offset:6144
	v_mfma_f32_16x16x32_f16 v[34:37], v[170:173], v[162:165], v[34:37]
	s_cmp_gt_u32 s53, 7
	s_cbranch_scc1 .Lc4_np5
	s_bitcmp1_b32 s53, 0
	s_cselect_b32 s56, 0xc000, 0
	s_add_i32 m0, s56, s43
	v_mad_u64_u32 v[118:119], s[76:77], v196, s53, v[184:185]
	global_load_lds_dwordx4 v[118:119], off
	s_add_i32 m0, s56, s44
	v_mad_u64_u32 v[118:119], s[76:77], v197, s53, v[186:187]
	global_load_lds_dwordx4 v[118:119], off
	s_add_i32 m0, s56, s45
	v_mad_u64_u32 v[118:119], s[76:77], v198, s53, v[188:189]
	global_load_lds_dwordx4 v[118:119], off
	s_add_i32 m0, s56, s46
	v_mad_u64_u32 v[118:119], s[76:77], v199, s53, v[190:191]
	global_load_lds_dwordx4 v[118:119], off
	s_add_i32 m0, s56, s47
	v_mad_u64_u32 v[118:119], s[76:77], v200, s53, v[192:193]
	global_load_lds_dwordx4 v[118:119], off
	s_add_i32 m0, s56, s50
	v_mad_u64_u32 v[118:119], s[76:77], v201, s53, v[194:195]
	global_load_lds_dwordx4 v[118:119], off
	s_add_i32 s53, s53, 1
	s_mov_b32 s67, 2

.Lc4_bar_6:
	s_barrier
	s_waitcnt lgkmcnt(5)
	v_mfma_f32_16x16x32_f16 v[110:113], v[62:65], v[70:73], v[110:113]
	ds_read_b128 v[142:145], v174
	s_mul_i32 s79, s49, 3
	s_add_i32 s79, s79, 18
	s_add_i32 s79, s79, s78
	s_lshl_b32 s68, s79, 15
	s_waitcnt lgkmcnt(5)
	v_mfma_f32_16x16x32_f16 v[106:109], v[58:61], v[70:73], v[106:109]
	v_add_u32_e32 v182, 69, v123
	v_bitop3_b32 v183, v182, v122, 6 bitop3:0x6c
	v_lshl_add_u32 v182, v182, 7, s80
	v_mfma_f32_16x16x32_f16 v[94:97], v[62:65], v[66:69], v[94:97]
	ds_read_b128 v[146:149], v174 offset:2048
	v_lshl_add_u64 v[178:179], v[116:117], 0, s[68:69]
	s_add_i32 s70, s38, 0xc000
	s_and_b32 s70, s70, 0xc000
	s_add_i32 s70, s70, s52
	v_mfma_f32_16x16x32_f16 v[74:77], v[58:61], v[66:69], v[74:77]
	v_lshl_or_b32 v176, v183, 4, v182
	v_xor_b32_e32 v176, s81, v176
	s_waitcnt lgkmcnt(5)
	v_mfma_f32_16x16x32_f16 v[42:45], v[62:65], v[82:85], v[42:45]
	ds_read_b128 v[150:153], v176
	v_mfma_f32_16x16x32_f16 v[26:29], v[58:61], v[82:85], v[26:29]
	v_add_u32_e32 v182, 103, v123
	v_bitop3_b32 v183, v182, v122, 6 bitop3:0x6c
	v_lshl_add_u32 v182, v182, 7, s80
	s_waitcnt lgkmcnt(5)
	v_mfma_f32_16x16x32_f16 v[46:49], v[62:65], v[78:81], v[46:49]
	ds_read_b128 v[154:157], v176 offset:2048
	v_mfma_f32_16x16x32_f16 v[30:33], v[58:61], v[78:81], v[30:33]
	v_lshl_or_b32 v177, v183, 4, v182
	v_xor_b32_e32 v177, s81, v177
	s_mov_b32 m0, s70
	s_add_i32 s71, s38, 0x4000
	global_load_lds_dwordx4 v[178:179], off
	s_waitcnt lgkmcnt(5)
	v_mfma_f32_16x16x32_f16 v[102:105], v[90:93], v[70:73], v[102:105]
	ds_read_b128 v[158:161], v177
	s_waitcnt lgkmcnt(5)
	v_mfma_f32_16x16x32_f16 v[98:101], v[86:89], v[70:73], v[98:101]
	s_and_b32 s71, s71, 0xc000
	s_add_i32 s72, s70, 0x400
	v_lshl_add_u64 v[180:181], v[178:179], 0, s[34:35]
	v_mfma_f32_16x16x32_f16 v[54:57], v[90:93], v[66:69], v[54:57]
	ds_read_b128 v[162:165], v177 offset:2048
	v_mfma_f32_16x16x32_f16 v[50:53], v[86:89], v[66:69], v[50:53]
	v_add_u32_e32 v175, s71, v204
	v_mfma_f32_16x16x32_f16 v[22:25], v[90:93], v[82:85], v[22:25]
	ds_read_b128 v[166:169], v174 offset:4096
	v_mfma_f32_16x16x32_f16 v[18:21], v[86:89], v[82:85], v[18:21]
	v_mfma_f32_16x16x32_f16 v[38:41], v[90:93], v[78:81], v[38:41]
	ds_read_b128 v[170:173], v174 offset:6144
	v_mfma_f32_16x16x32_f16 v[34:37], v[86:89], v[78:81], v[34:37]
	v_add_u32_e32 v174, s71, v205
	s_waitcnt lgkmcnt(7)
	v_mfma_f32_16x16x32_f16 v[110:113], v[142:145], v[82:85], v[110:113]
	ds_read_b128 v[62:65], v175
	s_waitcnt lgkmcnt(7)
	v_mfma_f32_16x16x32_f16 v[106:109], v[146:149], v[82:85], v[106:109]
	v_add_u32_e32 v182, 2, v123
	v_bitop3_b32 v183, v182, v122, 6 bitop3:0x6c
	v_lshl_add_u32 v182, v182, 7, s80
	v_mfma_f32_16x16x32_f16 v[94:97], v[142:145], v[78:81], v[94:97]
	ds_read_b128 v[58:61], v175 offset:2048
	v_mfma_f32_16x16x32_f16 v[74:77], v[146:149], v[78:81], v[74:77]
	v_lshl_or_b32 v176, v183, 4, v182
	v_xor_b32_e32 v176, s81, v176
	s_waitcnt lgkmcnt(7)
	v_mfma_f32_16x16x32_f16 v[42:45], v[142:145], v[150:153], v[42:45]
	ds_read_b128 v[70:73], v176
	v_mfma_f32_16x16x32_f16 v[26:29], v[146:149], v[150:153], v[26:29]
	s_waitcnt lgkmcnt(7)
	v_mfma_f32_16x16x32_f16 v[46:49], v[142:145], v[154:157], v[46:49]
	ds_read_b128 v[66:69], v176 offset:2048
	v_mfma_f32_16x16x32_f16 v[30:33], v[146:149], v[154:157], v[30:33]
	s_mov_b32 m0, s72
	s_addk_i32 s38, 0x4000
	global_load_lds_dwordx4 v[180:181], off
	s_waitcnt lgkmcnt(5)
	v_mfma_f32_16x16x32_f16 v[102:105], v[166:169], v[82:85], v[102:105]
	s_waitcnt lgkmcnt(4)
	v_mfma_f32_16x16x32_f16 v[98:101], v[170:173], v[82:85], v[98:101]
	v_mfma_f32_16x16x32_f16 v[54:57], v[166:169], v[78:81], v[54:57]
	v_mfma_f32_16x16x32_f16 v[50:53], v[170:173], v[78:81], v[50:53]
	v_mfma_f32_16x16x32_f16 v[22:25], v[166:169], v[150:153], v[22:25]
	ds_read_b128 v[90:93], v175 offset:4096
	v_mfma_f32_16x16x32_f16 v[18:21], v[170:173], v[150:153], v[18:21]
	v_mfma_f32_16x16x32_f16 v[38:41], v[166:169], v[154:157], v[38:41]
	ds_read_b128 v[86:89], v175 offset:6144
	v_mfma_f32_16x16x32_f16 v[34:37], v[170:173], v[154:157], v[34:37]
	s_cmp_eq_u32 s67, 0
	s_cbranch_scc1 .Lc4_w2_7
	s_waitcnt vmcnt(8)
	s_sub_i32 s67, s67, 1
	s_branch .Lc4_bar_7

.Lc4_bar_7:
	s_barrier
	s_waitcnt lgkmcnt(5)
	v_mfma_f32_16x16x32_f16 v[110:113], v[62:65], v[150:153], v[110:113]
	ds_read_b128 v[142:145], v174
	s_mul_i32 s79, s49, -5
	s_add_i32 s79, s79, 24
	s_add_i32 s79, s79, s78
	s_lshl_b32 s68, s79, 15
	s_waitcnt lgkmcnt(5)
	v_mfma_f32_16x16x32_f16 v[106:109], v[58:61], v[150:153], v[106:109]
	v_add_u32_e32 v182, 36, v123
	v_bitop3_b32 v183, v182, v122, 6 bitop3:0x6c
	v_lshl_add_u32 v182, v182, 7, s80
	v_mfma_f32_16x16x32_f16 v[94:97], v[62:65], v[154:157], v[94:97]
	ds_read_b128 v[146:149], v174 offset:2048
	v_lshl_add_u64 v[178:179], v[116:117], 0, s[68:69]
	s_add_i32 s70, s38, 0xc000
	s_and_b32 s70, s70, 0xc000
	s_add_i32 s70, s70, s52
	v_mfma_f32_16x16x32_f16 v[74:77], v[58:61], v[154:157], v[74:77]
	v_lshl_or_b32 v176, v183, 4, v182
	v_xor_b32_e32 v176, s81, v176
	v_mfma_f32_16x16x32_f16 v[42:45], v[62:65], v[158:161], v[42:45]
	ds_read_b128 v[82:85], v176
	v_mfma_f32_16x16x32_f16 v[26:29], v[58:61], v[158:161], v[26:29]
	v_mfma_f32_16x16x32_f16 v[46:49], v[62:65], v[162:165], v[46:49]
	ds_read_b128 v[78:81], v176 offset:2048
	v_mfma_f32_16x16x32_f16 v[30:33], v[58:61], v[162:165], v[30:33]
	s_mov_b32 m0, s70
	s_add_i32 s71, s38, 0x4000
	global_load_lds_dwordx4 v[178:179], off
	s_waitcnt lgkmcnt(5)
	v_mfma_f32_16x16x32_f16 v[102:105], v[90:93], v[150:153], v[102:105]
	s_waitcnt lgkmcnt(4)
	v_mfma_f32_16x16x32_f16 v[98:101], v[86:89], v[150:153], v[98:101]
	s_and_b32 s71, s71, 0xc000
	s_add_i32 s72, s70, 0x400
	v_lshl_add_u64 v[180:181], v[178:179], 0, s[34:35]
	v_mfma_f32_16x16x32_f16 v[54:57], v[90:93], v[154:157], v[54:57]
	v_mfma_f32_16x16x32_f16 v[50:53], v[86:89], v[154:157], v[50:53]
	v_add_u32_e32 v175, s71, v204
	v_mfma_f32_16x16x32_f16 v[22:25], v[90:93], v[158:161], v[22:25]
	ds_read_b128 v[166:169], v174 offset:4096
	v_mfma_f32_16x16x32_f16 v[18:21], v[86:89], v[158:161], v[18:21]
	v_mfma_f32_16x16x32_f16 v[38:41], v[90:93], v[162:165], v[38:41]
	ds_read_b128 v[170:173], v174 offset:6144
	v_mfma_f32_16x16x32_f16 v[34:37], v[86:89], v[162:165], v[34:37]
	v_add_u32_e32 v174, s71, v205
	s_waitcnt lgkmcnt(5)
	v_mfma_f32_16x16x32_f16 v[110:113], v[142:145], v[70:73], v[110:113]
	ds_read_b128 v[62:65], v175
	s_waitcnt lgkmcnt(5)
	v_mfma_f32_16x16x32_f16 v[106:109], v[146:149], v[70:73], v[106:109]
	v_add_u32_e32 v182, 70, v123
	v_bitop3_b32 v183, v182, v122, 6 bitop3:0x6c
	v_lshl_add_u32 v182, v182, 7, s80
	v_mfma_f32_16x16x32_f16 v[94:97], v[142:145], v[66:69], v[94:97]
	ds_read_b128 v[58:61], v175 offset:2048
	v_mfma_f32_16x16x32_f16 v[74:77], v[146:149], v[66:69], v[74:77]
	v_lshl_or_b32 v176, v183, 4, v182
	v_xor_b32_e32 v176, s81, v176
	s_waitcnt lgkmcnt(5)
	v_mfma_f32_16x16x32_f16 v[42:45], v[142:145], v[82:85], v[42:45]
	ds_read_b128 v[150:153], v176
	v_mfma_f32_16x16x32_f16 v[26:29], v[146:149], v[82:85], v[26:29]
	v_add_u32_e32 v182, 104, v123
	v_bitop3_b32 v183, v182, v122, 6 bitop3:0x6c
	v_lshl_add_u32 v182, v182, 7, s80
	s_waitcnt lgkmcnt(5)
	v_mfma_f32_16x16x32_f16 v[46:49], v[142:145], v[78:81], v[46:49]
	ds_read_b128 v[154:157], v176 offset:2048
	v_mfma_f32_16x16x32_f16 v[30:33], v[146:149], v[78:81], v[30:33]
	v_lshl_or_b32 v177, v183, 4, v182
	v_xor_b32_e32 v177, s81, v177
	s_mov_b32 m0, s72
	s_addk_i32 s38, 0x4000
	global_load_lds_dwordx4 v[180:181], off
	s_waitcnt lgkmcnt(5)
	v_mfma_f32_16x16x32_f16 v[102:105], v[166:169], v[70:73], v[102:105]
	ds_read_b128 v[158:161], v177
	s_waitcnt lgkmcnt(5)
	v_mfma_f32_16x16x32_f16 v[98:101], v[170:173], v[70:73], v[98:101]
	v_mfma_f32_16x16x32_f16 v[54:57], v[166:169], v[66:69], v[54:57]
	ds_read_b128 v[162:165], v177 offset:2048
	v_mfma_f32_16x16x32_f16 v[50:53], v[170:173], v[66:69], v[50:53]
	v_mfma_f32_16x16x32_f16 v[22:25], v[166:169], v[82:85], v[22:25]
	ds_read_b128 v[90:93], v175 offset:4096
	v_mfma_f32_16x16x32_f16 v[18:21], v[170:173], v[82:85], v[18:21]
	v_mfma_f32_16x16x32_f16 v[38:41], v[166:169], v[78:81], v[38:41]
	ds_read_b128 v[86:89], v175 offset:6144
	v_mfma_f32_16x16x32_f16 v[34:37], v[170:173], v[78:81], v[34:37]
	s_cmp_eq_u32 s67, 0
	s_cbranch_scc1 .Lc4_w2_8
	s_waitcnt vmcnt(8)
	s_sub_i32 s67, s67, 1
	s_branch .Lc4_bar_8

.Lc4_bar_8:
	s_barrier
	s_waitcnt lgkmcnt(7)
	v_mfma_f32_16x16x32_f16 v[110:113], v[62:65], v[82:85], v[110:113]
	ds_read_b128 v[142:145], v174
	s_mul_i32 s79, s49, 3
	s_add_i32 s79, s79, 22
	s_add_i32 s79, s79, s78
	s_lshl_b32 s68, s79, 15
	s_waitcnt lgkmcnt(7)
	v_mfma_f32_16x16x32_f16 v[106:109], v[58:61], v[82:85], v[106:109]
	v_mov_b32_e32 v182, v123
	v_bitop3_b32 v183, v182, v122, 6 bitop3:0x6c
	v_lshl_add_u32 v182, v182, 7, 0
	v_mfma_f32_16x16x32_f16 v[94:97], v[62:65], v[78:81], v[94:97]
	ds_read_b128 v[146:149], v174 offset:2048
	v_lshl_add_u64 v[178:179], v[116:117], 0, s[68:69]
	s_add_i32 s70, s38, 0xc000
	s_and_b32 s70, s70, 0xc000
	s_add_i32 s70, s70, s52
	v_mfma_f32_16x16x32_f16 v[74:77], v[58:61], v[78:81], v[74:77]
	v_lshl_or_b32 v176, v183, 4, v182
	v_xor_b32_e32 v176, s81, v176
	s_waitcnt lgkmcnt(7)
	v_mfma_f32_16x16x32_f16 v[42:45], v[62:65], v[150:153], v[42:45]
	ds_read_b128 v[70:73], v176
	v_mfma_f32_16x16x32_f16 v[26:29], v[58:61], v[150:153], v[26:29]
	s_waitcnt lgkmcnt(7)
	v_mfma_f32_16x16x32_f16 v[46:49], v[62:65], v[154:157], v[46:49]
	ds_read_b128 v[66:69], v176 offset:2048
	v_mfma_f32_16x16x32_f16 v[30:33], v[58:61], v[154:157], v[30:33]
	s_mov_b32 m0, s70
	s_add_i32 s71, s38, 0x4000
	global_load_lds_dwordx4 v[178:179], off
	s_waitcnt lgkmcnt(5)
	v_mfma_f32_16x16x32_f16 v[102:105], v[90:93], v[82:85], v[102:105]
	s_waitcnt lgkmcnt(4)
	v_mfma_f32_16x16x32_f16 v[98:101], v[86:89], v[82:85], v[98:101]
	s_and_b32 s71, s71, 0xc000
	s_add_i32 s72, s70, 0x400
	v_lshl_add_u64 v[180:181], v[178:179], 0, s[34:35]
	v_mfma_f32_16x16x32_f16 v[54:57], v[90:93], v[78:81], v[54:57]
	v_mfma_f32_16x16x32_f16 v[50:53], v[86:89], v[78:81], v[50:53]
	v_add_u32_e32 v175, s71, v204
	v_mfma_f32_16x16x32_f16 v[22:25], v[90:93], v[150:153], v[22:25]
	ds_read_b128 v[166:169], v174 offset:4096
	v_mfma_f32_16x16x32_f16 v[18:21], v[86:89], v[150:153], v[18:21]
	v_mfma_f32_16x16x32_f16 v[38:41], v[90:93], v[154:157], v[38:41]
	ds_read_b128 v[170:173], v174 offset:6144
	v_mfma_f32_16x16x32_f16 v[34:37], v[86:89], v[154:157], v[34:37]
	v_add_u32_e32 v174, s71, v205
	s_waitcnt lgkmcnt(5)
	v_mfma_f32_16x16x32_f16 v[110:113], v[142:145], v[150:153], v[110:113]
	ds_read_b128 v[62:65], v175
	s_waitcnt lgkmcnt(5)
	v_mfma_f32_16x16x32_f16 v[106:109], v[146:149], v[150:153], v[106:109]
	v_add_u32_e32 v182, 34, v123
	v_bitop3_b32 v183, v182, v122, 6 bitop3:0x6c
	v_lshl_add_u32 v182, v182, 7, 0
	v_mfma_f32_16x16x32_f16 v[94:97], v[142:145], v[154:157], v[94:97]
	ds_read_b128 v[58:61], v175 offset:2048
	v_mfma_f32_16x16x32_f16 v[74:77], v[146:149], v[154:157], v[74:77]
	v_lshl_or_b32 v176, v183, 4, v182
	v_xor_b32_e32 v176, s81, v176
	v_mfma_f32_16x16x32_f16 v[42:45], v[142:145], v[158:161], v[42:45]
	ds_read_b128 v[82:85], v176
	v_mfma_f32_16x16x32_f16 v[26:29], v[146:149], v[158:161], v[26:29]
	v_mfma_f32_16x16x32_f16 v[46:49], v[142:145], v[162:165], v[46:49]
	ds_read_b128 v[78:81], v176 offset:2048
	v_mfma_f32_16x16x32_f16 v[30:33], v[146:149], v[162:165], v[30:33]
	s_mov_b32 m0, s72
	s_addk_i32 s38, 0x4000
	global_load_lds_dwordx4 v[180:181], off
	s_waitcnt lgkmcnt(5)
	v_mfma_f32_16x16x32_f16 v[102:105], v[166:169], v[150:153], v[102:105]
	s_waitcnt lgkmcnt(4)
	v_mfma_f32_16x16x32_f16 v[98:101], v[170:173], v[150:153], v[98:101]
	v_mfma_f32_16x16x32_f16 v[54:57], v[166:169], v[154:157], v[54:57]
	v_mfma_f32_16x16x32_f16 v[50:53], v[170:173], v[154:157], v[50:53]
	v_mfma_f32_16x16x32_f16 v[22:25], v[166:169], v[158:161], v[22:25]
	ds_read_b128 v[90:93], v175 offset:4096
	v_mfma_f32_16x16x32_f16 v[18:21], v[170:173], v[158:161], v[18:21]
	s_add_i32 s61, s61, 1
	s_add_i32 s78, s78, 18
	v_mfma_f32_16x16x32_f16 v[38:41], v[166:169], v[162:165], v[38:41]
	ds_read_b128 v[86:89], v175 offset:6144
	s_cmp_eq_u32 s61, 4
	v_mfma_f32_16x16x32_f16 v[34:37], v[170:173], v[162:165], v[34:37]
	s_cbranch_scc0 .Lc4_loop

	.amdhsa_kernel _Z6conv_kILi512ELi256ELi3ELi64ELi1ELi1ELb0EEvPKDF16_S1_PKfS3_PDF16_S4_S1_fS3_S3_S3_S3_
		.amdhsa_group_segment_fixed_size 163840
		.amdhsa_private_segment_fixed_size 0
		.amdhsa_kernarg_size 96
		.amdhsa_user_sgpr_count 2
		.amdhsa_user_sgpr_dispatch_ptr 0
		.amdhsa_user_sgpr_queue_ptr 0
		.amdhsa_user_sgpr_kernarg_segment_ptr 1
		.amdhsa_user_sgpr_dispatch_id 0
		.amdhsa_user_sgpr_kernarg_preload_length 0
		.amdhsa_user_sgpr_kernarg_preload_offset 0
		.amdhsa_user_sgpr_private_segment_size 0
		.amdhsa_uses_dynamic_stack 0
		.amdhsa_enable_private_segment 0
		.amdhsa_system_sgpr_workgroup_id_x 1
		.amdhsa_system_sgpr_workgroup_id_y 0
		.amdhsa_system_sgpr_workgroup_id_z 0
		.amdhsa_system_sgpr_workgroup_info 0
		.amdhsa_system_vgpr_workitem_id 0
		.amdhsa_next_free_vgpr 208
		.amdhsa_next_free_sgpr 96
		.amdhsa_accum_offset 208
		.amdhsa_reserve_vcc 1
		.amdhsa_float_round_mode_32 0
		.amdhsa_float_round_mode_16_64 0
		.amdhsa_float_denorm_mode_32 3
		.amdhsa_float_denorm_mode_16_64 3
		.amdhsa_dx10_clamp 1
		.amdhsa_ieee_mode 1
		.amdhsa_fp16_overflow 0
		.amdhsa_tg_split 0
		.amdhsa_exception_fp_ieee_invalid_op 0
		.amdhsa_exception_fp_denorm_src 0
		.amdhsa_exception_fp_ieee_div_zero 0
		.amdhsa_exception_fp_ieee_overflow 0
		.amdhsa_exception_fp_ieee_underflow 0
		.amdhsa_exception_fp_ieee_inexact 0
		.amdhsa_exception_int_div_zero 0
	.end_amdhsa_kernel

amdhsa.kernels:
  - .agpr_count:     0
    .args:
      - .actual_access:  read_only
        .address_space:  global
        .offset:         0
        .size:           8
        .value_kind:     global_buffer
      - .actual_access:  read_only
        .address_space:  global
        .offset:         8
        .size:           8
        .value_kind:     global_buffer
      - .actual_access:  read_only
        .address_space:  global
        .offset:         16
        .size:           8
        .value_kind:     global_buffer
      - .actual_access:  read_only
        .address_space:  global
        .offset:         24
        .size:           8
        .value_kind:     global_buffer
      - .actual_access:  read_only
        .address_space:  global
        .offset:         32
        .size:           8
        .value_kind:     global_buffer
      - .actual_access:  read_only
        .address_space:  global
        .offset:         40
        .size:           8
        .value_kind:     global_buffer
      - .actual_access:  write_only
        .address_space:  global
        .offset:         48
        .size:           8
        .value_kind:     global_buffer
      - .actual_access:  write_only
        .address_space:  global
        .offset:         56
        .size:           8
        .value_kind:     global_buffer
      - .actual_access:  write_only
        .address_space:  global
        .offset:         64
        .size:           8
        .value_kind:     global_buffer
      - .actual_access:  write_only
        .address_space:  global
        .offset:         72
        .size:           8
        .value_kind:     global_buffer
      - .actual_access:  write_only
        .address_space:  global
        .offset:         80
        .size:           8
        .value_kind:     global_buffer
      - .actual_access:  write_only
        .address_space:  global
        .offset:         88
        .size:           8
        .value_kind:     global_buffer
      - .actual_access:  read_only
        .address_space:  global
        .offset:         96
        .size:           8
        .value_kind:     global_buffer
      - .actual_access:  read_only
        .address_space:  global
        .offset:         104
        .size:           8
        .value_kind:     global_buffer
      - .actual_access:  read_only
        .address_space:  global
        .offset:         112
        .size:           8
        .value_kind:     global_buffer
      - .actual_access:  read_only
        .address_space:  global
        .offset:         120
        .size:           8
        .value_kind:     global_buffer
      - .actual_access:  write_only
        .address_space:  global
        .offset:         128
        .size:           8
        .value_kind:     global_buffer
      - .actual_access:  write_only
        .address_space:  global
        .offset:         136
        .size:           8
        .value_kind:     global_buffer
    .group_segment_fixed_size: 14400
    .kernarg_segment_align: 8
    .kernarg_segment_size: 144
    .language:       OpenCL C
    .language_version:
      - 2
      - 0
    .max_flat_workgroup_size: 256
    .name:           _Z10prep_all_kPKfS0_S0_S0_S0_S0_PDF16_S1_S1_S1_S1_S1_S0_S0_S0_S0_S1_Pj
    .private_segment_fixed_size: 0
    .sgpr_count:     27
    .sgpr_spill_count: 0
    .symbol:         _Z10prep_all_kPKfS0_S0_S0_S0_S0_PDF16_S1_S1_S1_S1_S1_S0_S0_S0_S0_S1_Pj.kd
    .uniform_work_group_size: 1
    .uses_dynamic_stack: false
    .vgpr_count:     64
    .vgpr_spill_count: 0
    .wavefront_size: 64
  - .agpr_count:     0
    .args:
      - .actual_access:  read_only
        .address_space:  global
        .offset:         0
        .size:           8
        .value_kind:     global_buffer
      - .actual_access:  read_only
        .address_space:  global
        .offset:         8
        .size:           8
        .value_kind:     global_buffer
      - .actual_access:  read_only
        .address_space:  global
        .offset:         16
        .size:           8
        .value_kind:     global_buffer
      - .actual_access:  read_only
        .address_space:  global
        .offset:         24
        .size:           8
        .value_kind:     global_buffer
      - .actual_access:  read_only
        .address_space:  global
        .offset:         32
        .size:           8
        .value_kind:     global_buffer
      - .actual_access:  read_only
        .address_space:  global
        .offset:         40
        .size:           8
        .value_kind:     global_buffer
      - .actual_access:  write_only
        .address_space:  global
        .offset:         48
        .size:           8
        .value_kind:     global_buffer
    .group_segment_fixed_size: 0
    .kernarg_segment_align: 8
    .kernarg_segment_size: 56
    .language:       OpenCL C
    .language_version:
      - 2
      - 0
    .max_flat_workgroup_size: 256
    .name:           _Z9finish6_kPKDF16_PKfS2_S2_S2_S2_Pf
    .private_segment_fixed_size: 0
    .sgpr_count:     18
    .sgpr_spill_count: 0
    .symbol:         _Z9finish6_kPKDF16_PKfS2_S2_S2_S2_Pf.kd
    .uniform_work_group_size: 1
    .uses_dynamic_stack: false
    .vgpr_count:     51
    .vgpr_spill_count: 0
    .wavefront_size: 64
  - .agpr_count:     0
    .args:
      - .actual_access:  read_only
        .address_space:  global
        .offset:         0
        .size:           8
        .value_kind:     global_buffer
      - .actual_access:  write_only
        .address_space:  global
        .offset:         8
        .size:           8
        .value_kind:     global_buffer
    .group_segment_fixed_size: 16640
    .kernarg_segment_align: 8
    .kernarg_segment_size: 16
    .language:       OpenCL C
    .language_version:
      - 2
      - 0
    .max_flat_workgroup_size: 256
    .name:           _Z6gram_kPKfPf
    .private_segment_fixed_size: 0
    .sgpr_count:     16
    .sgpr_spill_count: 0
    .symbol:         _Z6gram_kPKfPf.kd
    .uniform_work_group_size: 1
    .uses_dynamic_stack: false
    .vgpr_count:     38
    .vgpr_spill_count: 0
    .wavefront_size: 64
  - .agpr_count:     0
    .args:
      - .actual_access:  read_only
        .address_space:  global
        .offset:         0
        .size:           8
        .value_kind:     global_buffer
      - .address_space:  global
        .offset:         8
        .size:           8
        .value_kind:     global_buffer
      - .actual_access:  read_only
        .address_space:  global
        .offset:         16
        .size:           8
        .value_kind:     global_buffer
      - .actual_access:  read_only
        .address_space:  global
        .offset:         24
        .size:           8
        .value_kind:     global_buffer
      - .actual_access:  read_only
        .address_space:  global
        .offset:         32
        .size:           8
        .value_kind:     global_buffer
      - .actual_access:  write_only
        .address_space:  global
        .offset:         40
        .size:           8
        .value_kind:     global_buffer
      - .actual_access:  read_only
        .address_space:  global
        .offset:         48
        .size:           8
        .value_kind:     global_buffer
      - .offset:         56
        .size:           4
        .value_kind:     by_value
      - .actual_access:  read_only
        .address_space:  global
        .offset:         64
        .size:           8
        .value_kind:     global_buffer
      - .actual_access:  read_only
        .address_space:  global
        .offset:         72
        .size:           8
        .value_kind:     global_buffer
      - .actual_access:  read_only
        .address_space:  global
        .offset:         80
        .size:           8
        .value_kind:     global_buffer
      - .actual_access:  read_only
        .address_space:  global
        .offset:         88
        .size:           8
        .value_kind:     global_buffer
    .group_segment_fixed_size: 147456
    .kernarg_segment_align: 8
    .kernarg_segment_size: 96
    .language:       OpenCL C
    .language_version:
      - 2
      - 0
    .max_flat_workgroup_size: 512
    .name:           _Z6conv_kILi64ELi128ELi20ELi128ELi4ELi4ELb1EEvPKDF16_S1_PKfS3_PDF16_S4_S1_fS3_S3_S3_S3_
    .private_segment_fixed_size: 0
    .sgpr_count:     43
    .sgpr_spill_count: 0
    .symbol:         _Z6conv_kILi64ELi128ELi20ELi128ELi4ELi4ELb1EEvPKDF16_S1_PKfS3_PDF16_S4_S1_fS3_S3_S3_S3_.kd
    .uniform_work_group_size: 1
    .uses_dynamic_stack: false
    .vgpr_count:     160
    .vgpr_spill_count: 0
    .wavefront_size: 64
  - .agpr_count:     0
    .args:
      - .actual_access:  read_only
        .address_space:  global
        .offset:         0
        .size:           8
        .value_kind:     global_buffer
      - .actual_access:  read_only
        .address_space:  global
        .offset:         8
        .size:           8
        .value_kind:     global_buffer
      - .actual_access:  read_only
        .address_space:  global
        .offset:         16
        .size:           8
        .value_kind:     global_buffer
      - .actual_access:  write_only
        .address_space:  global
        .offset:         24
        .size:           8
        .value_kind:     global_buffer
    .group_segment_fixed_size: 0
    .kernarg_segment_align: 8
    .kernarg_segment_size: 32
    .language:       OpenCL C
    .language_version:
      - 2
      - 0
    .max_flat_workgroup_size: 256
    .name:           _Z8finish_kILi128ELi4EEvPKDF16_PKfS3_PDF16_
    .private_segment_fixed_size: 0
    .sgpr_count:     18
    .sgpr_spill_count: 0
    .symbol:         _Z8finish_kILi128ELi4EEvPKDF16_PKfS3_PDF16_.kd
    .uniform_work_group_size: 1
    .uses_dynamic_stack: false
    .vgpr_count:     44
    .vgpr_spill_count: 0
    .wavefront_size: 64
  - .agpr_count:     0
    .args:
      - .address_space:  global
        .offset:         0
        .size:           8
        .value_kind:     global_buffer
      - .address_space:  global
        .offset:         8
        .size:           8
        .value_kind:     global_buffer
      - .address_space:  global
        .offset:         16
        .size:           8
        .value_kind:     global_buffer
      - .actual_access:  read_only
        .address_space:  global
        .offset:         24
        .size:           8
        .value_kind:     global_buffer
      - .actual_access:  write_only
        .address_space:  global
        .offset:         32
        .size:           8
        .value_kind:     global_buffer
      - .actual_access:  read_only
        .address_space:  global
        .offset:         40
        .size:           8
        .value_kind:     global_buffer
      - .address_space:  global
        .offset:         48
        .size:           8
        .value_kind:     global_buffer
      - .offset:         56
        .size:           4
        .value_kind:     by_value
      - .actual_access:  read_only
        .address_space:  global
        .offset:         64
        .size:           8
        .value_kind:     global_buffer
      - .actual_access:  read_only
        .address_space:  global
        .offset:         72
        .size:           8
        .value_kind:     global_buffer
      - .actual_access:  read_only
        .address_space:  global
        .offset:         80
        .size:           8
        .value_kind:     global_buffer
      - .actual_access:  read_only
        .address_space:  global
        .offset:         88
        .size:           8
        .value_kind:     global_buffer
    .group_segment_fixed_size: 163840
    .kernarg_segment_align: 8
    .kernarg_segment_size: 96
    .language:       OpenCL C
    .language_version:
      - 2
      - 0
    .max_flat_workgroup_size: 512
    .name:           _Z6conv_kILi128ELi256ELi3ELi64ELi1ELi1ELb0EEvPKDF16_S1_PKfS3_PDF16_S4_S1_fS3_S3_S3_S3_
    .private_segment_fixed_size: 0
    .sgpr_count:     51
    .sgpr_spill_count: 0
    .symbol:         _Z6conv_kILi128ELi256ELi3ELi64ELi1ELi1ELb0EEvPKDF16_S1_PKfS3_PDF16_S4_S1_fS3_S3_S3_S3_.kd
    .uniform_work_group_size: 1
    .uses_dynamic_stack: false
    .vgpr_count:     184
    .vgpr_spill_count: 0
    .wavefront_size: 64
  - .agpr_count:     0
    .args:
      - .address_space:  global
        .offset:         0
        .size:           8
        .value_kind:     global_buffer
      - .address_space:  global
        .offset:         8
        .size:           8
        .value_kind:     global_buffer
      - .address_space:  global
        .offset:         16
        .size:           8
        .value_kind:     global_buffer
      - .actual_access:  read_only
        .address_space:  global
        .offset:         24
        .size:           8
        .value_kind:     global_buffer
      - .actual_access:  write_only
        .address_space:  global
        .offset:         32
        .size:           8
        .value_kind:     global_buffer
      - .actual_access:  read_only
        .address_space:  global
        .offset:         40
        .size:           8
        .value_kind:     global_buffer
      - .address_space:  global
        .offset:         48
        .size:           8
        .value_kind:     global_buffer
      - .offset:         56
        .size:           4
        .value_kind:     by_value
      - .actual_access:  read_only
        .address_space:  global
        .offset:         64
        .size:           8
        .value_kind:     global_buffer
      - .actual_access:  read_only
        .address_space:  global
        .offset:         72
        .size:           8
        .value_kind:     global_buffer
      - .actual_access:  read_only
        .address_space:  global
        .offset:         80
        .size:           8
        .value_kind:     global_buffer
      - .actual_access:  read_only
        .address_space:  global
        .offset:         88
        .size:           8
        .value_kind:     global_buffer
    .group_segment_fixed_size: 163840
    .kernarg_segment_align: 8
    .kernarg_segment_size: 96
    .language:       OpenCL C
    .language_version:
      - 2
      - 0
    .max_flat_workgroup_size: 512
    .name:           _Z6conv_kILi256ELi512ELi3ELi128ELi1ELi1ELb0EEvPKDF16_S1_PKfS3_PDF16_S4_S1_fS3_S3_S3_S3_
    .private_segment_fixed_size: 0
    .sgpr_count:     64
    .sgpr_spill_count: 0
    .symbol:         _Z6conv_kILi256ELi512ELi3ELi128ELi1ELi1ELb0EEvPKDF16_S1_PKfS3_PDF16_S4_S1_fS3_S3_S3_S3_.kd
    .uniform_work_group_size: 1
    .uses_dynamic_stack: false
    .vgpr_count:     184
    .vgpr_spill_count: 0
    .wavefront_size: 64
  - .agpr_count:     0
    .args:
      - .address_space:  global
        .offset:         0
        .size:           8
        .value_kind:     global_buffer
      - .address_space:  global
        .offset:         8
        .size:           8
        .value_kind:     global_buffer
      - .address_space:  global
        .offset:         16
        .size:           8
        .value_kind:     global_buffer
      - .actual_access:  read_only
        .address_space:  global
        .offset:         24
        .size:           8
        .value_kind:     global_buffer
      - .actual_access:  write_only
        .address_space:  global
        .offset:         32
        .size:           8
        .value_kind:     global_buffer
      - .actual_access:  read_only
        .address_space:  global
        .offset:         40
        .size:           8
        .value_kind:     global_buffer
      - .address_space:  global
        .offset:         48
        .size:           8
        .value_kind:     global_buffer
      - .offset:         56
        .size:           4
        .value_kind:     by_value
      - .actual_access:  read_only
        .address_space:  global
        .offset:         64
        .size:           8
        .value_kind:     global_buffer
      - .actual_access:  read_only
        .address_space:  global
        .offset:         72
        .size:           8
        .value_kind:     global_buffer
      - .actual_access:  read_only
        .address_space:  global
        .offset:         80
        .size:           8
        .value_kind:     global_buffer
      - .actual_access:  read_only
        .address_space:  global
        .offset:         88
        .size:           8
        .value_kind:     global_buffer
    .group_segment_fixed_size: 163840
    .kernarg_segment_align: 8
    .kernarg_segment_size: 96
    .language:       OpenCL C
    .language_version:
      - 2
      - 0
    .max_flat_workgroup_size: 512
    .name:           _Z6conv_kILi512ELi256ELi3ELi64ELi1ELi1ELb0EEvPKDF16_S1_PKfS3_PDF16_S4_S1_fS3_S3_S3_S3_
    .private_segment_fixed_size: 0
    .sgpr_count:     66
    .sgpr_spill_count: 0
    .symbol:         _Z6conv_kILi512ELi256ELi3ELi64ELi1ELi1ELb0EEvPKDF16_S1_PKfS3_PDF16_S4_S1_fS3_S3_S3_S3_.kd
    .uniform_work_group_size: 1
    .uses_dynamic_stack: false
    .vgpr_count:     208
    .vgpr_spill_count: 0
    .wavefront_size: 64
  - .agpr_count:     0
    .args:
      - .address_space:  global
        .offset:         0
        .size:           8
        .value_kind:     global_buffer
      - .address_space:  global
        .offset:         8
        .size:           8
        .value_kind:     global_buffer
      - .actual_access:  read_only
        .address_space:  global
        .offset:         16
        .size:           8
        .value_kind:     global_buffer
      - .actual_access:  read_only
        .address_space:  global
        .offset:         24
        .size:           8
        .value_kind:     global_buffer
      - .actual_access:  read_only
        .address_space:  global
        .offset:         32
        .size:           8
        .value_kind:     global_buffer
      - .actual_access:  write_only
        .address_space:  global
        .offset:         40
        .size:           8
        .value_kind:     global_buffer
      - .address_space:  global
        .offset:         48
        .size:           8
        .value_kind:     global_buffer
      - .offset:         56
        .size:           4
        .value_kind:     by_value
      - .actual_access:  read_only
        .address_space:  global
        .offset:         64
        .size:           8
        .value_kind:     global_buffer
      - .actual_access:  read_only
        .address_space:  global
        .offset:         72
        .size:           8
        .value_kind:     global_buffer
      - .actual_access:  read_only
        .address_space:  global
        .offset:         80
        .size:           8
        .value_kind:     global_buffer
      - .actual_access:  read_only
        .address_space:  global
        .offset:         88
        .size:           8
        .value_kind:     global_buffer
    .group_segment_fixed_size: 163840
    .kernarg_segment_align: 8
    .kernarg_segment_size: 96
    .language:       OpenCL C
    .language_version:
      - 2
      - 0
    .max_flat_workgroup_size: 512
    .name:           _Z6conv_kILi256ELi128ELi3ELi64ELi1ELi2ELb0EEvPKDF16_S1_PKfS3_PDF16_S4_S1_fS3_S3_S3_S3_
    .private_segment_fixed_size: 0
    .sgpr_count:     55
    .sgpr_spill_count: 0
    .symbol:         _Z6conv_kILi256ELi128ELi3ELi64ELi1ELi2ELb0EEvPKDF16_S1_PKfS3_PDF16_S4_S1_fS3_S3_S3_S3_.kd
    .uniform_work_group_size: 1
    .uses_dynamic_stack: false
    .vgpr_count:     172
    .vgpr_spill_count: 0
    .wavefront_size: 64
  - .agpr_count:     0
    .args:
      - .actual_access:  read_only
        .address_space:  global
        .offset:         0
        .size:           8
        .value_kind:     global_buffer
      - .actual_access:  read_only
        .address_space:  global
        .offset:         8
        .size:           8
        .value_kind:     global_buffer
      - .actual_access:  read_only
        .address_space:  global
        .offset:         16
        .size:           8
        .value_kind:     global_buffer
      - .actual_access:  write_only
        .address_space:  global
        .offset:         24
        .size:           8
        .value_kind:     global_buffer
    .group_segment_fixed_size: 0
    .kernarg_segment_align: 8
    .kernarg_segment_size: 32
    .language:       OpenCL C
    .language_version:
      - 2
      - 0
    .max_flat_workgroup_size: 256
    .name:           _Z8finish_kILi128ELi2EEvPKDF16_PKfS3_PDF16_
    .private_segment_fixed_size: 0
    .sgpr_count:     18
    .sgpr_spill_count: 0
    .symbol:         _Z8finish_kILi128ELi2EEvPKDF16_PKfS3_PDF16_.kd
    .uniform_work_group_size: 1
    .uses_dynamic_stack: false
    .vgpr_count:     28
    .vgpr_spill_count: 0
    .wavefront_size: 64
  - .agpr_count:     0
    .args:
      - .address_space:  global
        .offset:         0
        .size:           8
        .value_kind:     global_buffer
      - .address_space:  global
        .offset:         8
        .size:           8
        .value_kind:     global_buffer
      - .actual_access:  read_only
        .address_space:  global
        .offset:         16
        .size:           8
        .value_kind:     global_buffer
      - .actual_access:  read_only
        .address_space:  global
        .offset:         24
        .size:           8
        .value_kind:     global_buffer
      - .actual_access:  read_only
        .address_space:  global
        .offset:         32
        .size:           8
        .value_kind:     global_buffer
      - .actual_access:  write_only
        .address_space:  global
        .offset:         40
        .size:           8
        .value_kind:     global_buffer
      - .address_space:  global
        .offset:         48
        .size:           8
        .value_kind:     global_buffer
      - .offset:         56
        .size:           4
        .value_kind:     by_value
      - .actual_access:  read_only
        .address_space:  global
        .offset:         64
        .size:           8
        .value_kind:     global_buffer
      - .actual_access:  read_only
        .address_space:  global
        .offset:         72
        .size:           8
        .value_kind:     global_buffer
      - .actual_access:  read_only
        .address_space:  global
        .offset:         80
        .size:           8
        .value_kind:     global_buffer
      - .actual_access:  read_only
        .address_space:  global
        .offset:         88
        .size:           8
        .value_kind:     global_buffer
    .group_segment_fixed_size: 147456
    .kernarg_segment_align: 8
    .kernarg_segment_size: 96
    .language:       OpenCL C
    .language_version:
      - 2
      - 0
    .max_flat_workgroup_size: 512
    .name:           _Z6conv_kILi128ELi64ELi20ELi64ELi4ELi4ELb0EEvPKDF16_S1_PKfS3_PDF16_S4_S1_fS3_S3_S3_S3_
    .private_segment_fixed_size: 0
    .sgpr_count:     64
    .sgpr_spill_count: 0
    .symbol:         _Z6conv_kILi128ELi64ELi20ELi64ELi4ELi4ELb0EEvPKDF16_S1_PKfS3_PDF16_S4_S1_fS3_S3_S3_S3_.kd
    .uniform_work_group_size: 1
    .uses_dynamic_stack: false
    .vgpr_count:     184
    .vgpr_spill_count: 0
    .wavefront_size: 64
